# layer1: MFMA steps 0-3 overlap the self-row loads (single-buffered W frags); layer2 ring of 4 loads
# speedup vs baseline: 1.3369x; 1.0128x over previous
.Lg1_final:
	v_max_i32_e32 v94, 1, v78
	v_cvt_f32_u32_e32 v94, v94
	v_div_scale_f32 v96, s[62:63], v94, v94, 1.0
	v_rcp_f32_e32 v97, v96
	v_div_scale_f32 v98, vcc, 1.0, v94, 1.0
	v_fma_f32 v99, -v96, v97, 1.0
	v_fmac_f32_e32 v97, v99, v97
	v_mul_f32_e32 v99, v98, v97
	v_fma_f32 v95, -v96, v99, v98
	v_fmac_f32_e32 v99, v95, v97
	v_fma_f32 v96, -v96, v99, v98
	v_div_fmas_f32 v96, v96, v97, v99
	v_div_fixup_f32 v95, v96, v94, 1.0
	v_mul_f32_e32 v18, 0x43000000, v18
	v_sub_f32_e32 v2, v2, v18
	v_sub_f32_e32 v3, v3, v18
	v_sub_f32_e32 v4, v4, v18
	v_sub_f32_e32 v5, v5, v18
	v_sub_f32_e32 v6, v6, v18
	v_sub_f32_e32 v7, v7, v18
	v_sub_f32_e32 v8, v8, v18
	v_sub_f32_e32 v9, v9, v18
	v_sub_f32_e32 v10, v10, v18
	v_sub_f32_e32 v11, v11, v18
	v_sub_f32_e32 v12, v12, v18
	v_sub_f32_e32 v13, v13, v18
	v_sub_f32_e32 v14, v14, v18
	v_sub_f32_e32 v15, v15, v18
	v_sub_f32_e32 v16, v16, v18
	v_sub_f32_e32 v17, v17, v18
	v_mul_f32_e32 v2, v95, v2
	v_mul_f32_e32 v3, v95, v3
	v_mul_f32_e32 v4, v95, v4
	v_mul_f32_e32 v5, v95, v5
	v_mul_f32_e32 v6, v95, v6
	v_mul_f32_e32 v7, v95, v7
	v_mul_f32_e32 v8, v95, v8
	v_mul_f32_e32 v9, v95, v9
	v_mul_f32_e32 v10, v95, v10
	v_mul_f32_e32 v11, v95, v11
	v_mul_f32_e32 v12, v95, v12
	v_mul_f32_e32 v13, v95, v13
	v_mul_f32_e32 v14, v95, v14
	v_mul_f32_e32 v15, v95, v15
	v_mul_f32_e32 v16, v95, v16
	v_mul_f32_e32 v17, v95, v17
	v_cvt_pk_f16_f32 v52, v2, v3
	v_cvt_pk_f16_f32 v53, v4, v5
	v_cvt_pk_f16_f32 v54, v6, v7
	v_cvt_pk_f16_f32 v55, v8, v9
	v_cvt_pk_f16_f32 v56, v10, v11
	v_cvt_pk_f16_f32 v57, v12, v13
	v_cvt_pk_f16_f32 v58, v14, v15
	v_cvt_pk_f16_f32 v59, v16, v17
	ds_write_b128 v93, v[52:55]
	ds_write_b128 v93, v[56:59] offset:16
	s_add_u32 s39, s39, 1
	s_cmp_lt_u32 s39, 2
	s_cbranch_scc1 .Lg1_set_top
	v_lshlrev_b32_e32 v107, 9, v105
	v_xor_b32_e32 v108, v106, v105
	v_lshlrev_b32_e32 v108, 4, v108
	v_mul_u32_u24_e32 v109, 0x110, v105
	v_lshl_add_u32 v109, v106, 4, v109
	v_add_u32_e32 v109, s48, v109
	v_lshlrev_b32_e32 v110, 4, v106
	v_add_u32_e32 v110, 0x10000, v110
	s_waitcnt lgkmcnt(0)
	ds_read_b128 v[52:55], v110 offset:0
	ds_read_b128 v[56:59], v110 offset:64
	ds_read_b128 v[60:63], v110 offset:128
	ds_read_b128 v[64:67], v110 offset:192
	ds_read_b128 v[68:71], v110 offset:256
	ds_read_b128 v[72:75], v110 offset:320
	ds_read_b128 v[76:79], v110 offset:384
	ds_read_b128 v[80:83], v110 offset:448
	v_xor_b32_e32 v111, 0, v108
	v_add_u32_e32 v111, v111, v107
	ds_read_b128 v[16:19], v109 offset:0
	ds_read_b128 v[84:87], v111 offset:0
	ds_read_b128 v[88:91], v111 offset:8192
	ds_read_b128 v[92:95], v111 offset:16384
	ds_read_b128 v[96:99], v111 offset:24576
	ds_read_b128 v[0:3], v111 offset:32768
	ds_read_b128 v[4:7], v111 offset:40960
	ds_read_b128 v[8:11], v111 offset:49152
	ds_read_b128 v[12:15], v111 offset:57344
	s_waitcnt lgkmcnt(0)
	v_mfma_f32_16x16x32_f16 v[52:55], v[84:87], v[16:19], v[52:55]
	v_mfma_f32_16x16x32_f16 v[56:59], v[88:91], v[16:19], v[56:59]
	v_mfma_f32_16x16x32_f16 v[60:63], v[92:95], v[16:19], v[60:63]
	v_mfma_f32_16x16x32_f16 v[64:67], v[96:99], v[16:19], v[64:67]
	v_mfma_f32_16x16x32_f16 v[68:71], v[0:3], v[16:19], v[68:71]
	v_mfma_f32_16x16x32_f16 v[72:75], v[4:7], v[16:19], v[72:75]
	v_mfma_f32_16x16x32_f16 v[76:79], v[8:11], v[16:19], v[76:79]
	v_mfma_f32_16x16x32_f16 v[80:83], v[12:15], v[16:19], v[80:83]
	v_xor_b32_e32 v111, 64, v108
	v_add_u32_e32 v111, v111, v107
	ds_read_b128 v[100:103], v109 offset:64
	ds_read_b128 v[84:87], v111 offset:0
	ds_read_b128 v[88:91], v111 offset:8192
	ds_read_b128 v[92:95], v111 offset:16384
	ds_read_b128 v[96:99], v111 offset:24576
	ds_read_b128 v[0:3], v111 offset:32768
	ds_read_b128 v[4:7], v111 offset:40960
	ds_read_b128 v[8:11], v111 offset:49152
	ds_read_b128 v[12:15], v111 offset:57344
	s_waitcnt lgkmcnt(0)
	v_mfma_f32_16x16x32_f16 v[52:55], v[84:87], v[100:103], v[52:55]
	v_mfma_f32_16x16x32_f16 v[56:59], v[88:91], v[100:103], v[56:59]
	v_mfma_f32_16x16x32_f16 v[60:63], v[92:95], v[100:103], v[60:63]
	v_mfma_f32_16x16x32_f16 v[64:67], v[96:99], v[100:103], v[64:67]
	v_mfma_f32_16x16x32_f16 v[68:71], v[0:3], v[100:103], v[68:71]
	v_mfma_f32_16x16x32_f16 v[72:75], v[4:7], v[100:103], v[72:75]
	v_mfma_f32_16x16x32_f16 v[76:79], v[8:11], v[100:103], v[76:79]
	v_mfma_f32_16x16x32_f16 v[80:83], v[12:15], v[100:103], v[80:83]
	v_xor_b32_e32 v111, 128, v108
	v_add_u32_e32 v111, v111, v107
	ds_read_b128 v[16:19], v109 offset:128
	ds_read_b128 v[84:87], v111 offset:0
	ds_read_b128 v[88:91], v111 offset:8192
	ds_read_b128 v[92:95], v111 offset:16384
	ds_read_b128 v[96:99], v111 offset:24576
	ds_read_b128 v[0:3], v111 offset:32768
	ds_read_b128 v[4:7], v111 offset:40960
	ds_read_b128 v[8:11], v111 offset:49152
	ds_read_b128 v[12:15], v111 offset:57344
	s_waitcnt lgkmcnt(0)
	v_mfma_f32_16x16x32_f16 v[52:55], v[84:87], v[16:19], v[52:55]
	v_mfma_f32_16x16x32_f16 v[56:59], v[88:91], v[16:19], v[56:59]
	v_mfma_f32_16x16x32_f16 v[60:63], v[92:95], v[16:19], v[60:63]
	v_mfma_f32_16x16x32_f16 v[64:67], v[96:99], v[16:19], v[64:67]
	v_mfma_f32_16x16x32_f16 v[68:71], v[0:3], v[16:19], v[68:71]
	v_mfma_f32_16x16x32_f16 v[72:75], v[4:7], v[16:19], v[72:75]
	v_mfma_f32_16x16x32_f16 v[76:79], v[8:11], v[16:19], v[76:79]
	v_mfma_f32_16x16x32_f16 v[80:83], v[12:15], v[16:19], v[80:83]
	v_xor_b32_e32 v111, 192, v108
	v_add_u32_e32 v111, v111, v107
	ds_read_b128 v[100:103], v109 offset:192
	ds_read_b128 v[84:87], v111 offset:0
	ds_read_b128 v[88:91], v111 offset:8192
	ds_read_b128 v[92:95], v111 offset:16384
	ds_read_b128 v[96:99], v111 offset:24576
	ds_read_b128 v[0:3], v111 offset:32768
	ds_read_b128 v[4:7], v111 offset:40960
	ds_read_b128 v[8:11], v111 offset:49152
	ds_read_b128 v[12:15], v111 offset:57344
	s_waitcnt lgkmcnt(0)
	v_mfma_f32_16x16x32_f16 v[52:55], v[84:87], v[100:103], v[52:55]
	v_mfma_f32_16x16x32_f16 v[56:59], v[88:91], v[100:103], v[56:59]
	v_mfma_f32_16x16x32_f16 v[60:63], v[92:95], v[100:103], v[60:63]
	v_mfma_f32_16x16x32_f16 v[64:67], v[96:99], v[100:103], v[64:67]
	v_mfma_f32_16x16x32_f16 v[68:71], v[0:3], v[100:103], v[68:71]
	v_mfma_f32_16x16x32_f16 v[72:75], v[4:7], v[100:103], v[72:75]
	v_mfma_f32_16x16x32_f16 v[76:79], v[8:11], v[100:103], v[76:79]
	v_mfma_f32_16x16x32_f16 v[80:83], v[12:15], v[100:103], v[80:83]
	s_waitcnt vmcnt(0)
	v_cvt_pk_f16_f32 v112, v20, v21
	v_cvt_pk_f16_f32 v113, v22, v23
	v_cvt_pk_f16_f32 v114, v24, v25
	v_cvt_pk_f16_f32 v115, v26, v27
	v_cvt_pk_f16_f32 v116, v28, v29
	v_cvt_pk_f16_f32 v117, v30, v31
	v_cvt_pk_f16_f32 v118, v32, v33
	v_cvt_pk_f16_f32 v119, v34, v35
	v_cvt_pk_f16_f32 v120, v36, v37
	v_cvt_pk_f16_f32 v121, v38, v39
	v_cvt_pk_f16_f32 v122, v40, v41
	v_cvt_pk_f16_f32 v123, v42, v43
	v_cvt_pk_f16_f32 v124, v44, v45
	v_cvt_pk_f16_f32 v125, v46, v47
	v_cvt_pk_f16_f32 v126, v48, v49
	v_cvt_pk_f16_f32 v127, v50, v51
	v_xor_b32_e32 v111, 256, v108
	v_add_u32_e32 v111, v111, v107
	ds_read_b128 v[84:87], v111 offset:0
	ds_read_b128 v[88:91], v111 offset:8192
	ds_read_b128 v[92:95], v111 offset:16384
	ds_read_b128 v[96:99], v111 offset:24576
	ds_read_b128 v[0:3], v111 offset:32768
	ds_read_b128 v[4:7], v111 offset:40960
	ds_read_b128 v[8:11], v111 offset:49152
	ds_read_b128 v[12:15], v111 offset:57344
	s_waitcnt lgkmcnt(0)
	v_mfma_f32_16x16x32_f16 v[52:55], v[84:87], v[112:115], v[52:55]
	v_mfma_f32_16x16x32_f16 v[56:59], v[88:91], v[112:115], v[56:59]
	v_mfma_f32_16x16x32_f16 v[60:63], v[92:95], v[112:115], v[60:63]
	v_mfma_f32_16x16x32_f16 v[64:67], v[96:99], v[112:115], v[64:67]
	v_mfma_f32_16x16x32_f16 v[68:71], v[0:3], v[112:115], v[68:71]
	v_mfma_f32_16x16x32_f16 v[72:75], v[4:7], v[112:115], v[72:75]
	v_mfma_f32_16x16x32_f16 v[76:79], v[8:11], v[112:115], v[76:79]
	v_mfma_f32_16x16x32_f16 v[80:83], v[12:15], v[112:115], v[80:83]
	v_xor_b32_e32 v111, 320, v108
	v_add_u32_e32 v111, v111, v107
	ds_read_b128 v[84:87], v111 offset:0
	ds_read_b128 v[88:91], v111 offset:8192
	ds_read_b128 v[92:95], v111 offset:16384
	ds_read_b128 v[96:99], v111 offset:24576
	ds_read_b128 v[0:3], v111 offset:32768
	ds_read_b128 v[4:7], v111 offset:40960
	ds_read_b128 v[8:11], v111 offset:49152
	ds_read_b128 v[12:15], v111 offset:57344
	s_waitcnt lgkmcnt(0)
	v_mfma_f32_16x16x32_f16 v[52:55], v[84:87], v[116:119], v[52:55]
	v_mfma_f32_16x16x32_f16 v[56:59], v[88:91], v[116:119], v[56:59]
	v_mfma_f32_16x16x32_f16 v[60:63], v[92:95], v[116:119], v[60:63]
	v_mfma_f32_16x16x32_f16 v[64:67], v[96:99], v[116:119], v[64:67]
	v_mfma_f32_16x16x32_f16 v[68:71], v[0:3], v[116:119], v[68:71]
	v_mfma_f32_16x16x32_f16 v[72:75], v[4:7], v[116:119], v[72:75]
	v_mfma_f32_16x16x32_f16 v[76:79], v[8:11], v[116:119], v[76:79]
	v_mfma_f32_16x16x32_f16 v[80:83], v[12:15], v[116:119], v[80:83]
	v_xor_b32_e32 v111, 384, v108
	v_add_u32_e32 v111, v111, v107
	ds_read_b128 v[84:87], v111 offset:0
	ds_read_b128 v[88:91], v111 offset:8192
	ds_read_b128 v[92:95], v111 offset:16384
	ds_read_b128 v[96:99], v111 offset:24576
	ds_read_b128 v[0:3], v111 offset:32768
	ds_read_b128 v[4:7], v111 offset:40960
	ds_read_b128 v[8:11], v111 offset:49152
	ds_read_b128 v[12:15], v111 offset:57344
	s_waitcnt lgkmcnt(0)
	v_mfma_f32_16x16x32_f16 v[52:55], v[84:87], v[120:123], v[52:55]
	v_mfma_f32_16x16x32_f16 v[56:59], v[88:91], v[120:123], v[56:59]
	v_mfma_f32_16x16x32_f16 v[60:63], v[92:95], v[120:123], v[60:63]
	v_mfma_f32_16x16x32_f16 v[64:67], v[96:99], v[120:123], v[64:67]
	v_mfma_f32_16x16x32_f16 v[68:71], v[0:3], v[120:123], v[68:71]
	v_mfma_f32_16x16x32_f16 v[72:75], v[4:7], v[120:123], v[72:75]
	v_mfma_f32_16x16x32_f16 v[76:79], v[8:11], v[120:123], v[76:79]
	v_mfma_f32_16x16x32_f16 v[80:83], v[12:15], v[120:123], v[80:83]
	v_xor_b32_e32 v111, 448, v108
	v_add_u32_e32 v111, v111, v107
	ds_read_b128 v[84:87], v111 offset:0
	ds_read_b128 v[88:91], v111 offset:8192
	ds_read_b128 v[92:95], v111 offset:16384
	ds_read_b128 v[96:99], v111 offset:24576
	ds_read_b128 v[0:3], v111 offset:32768
	ds_read_b128 v[4:7], v111 offset:40960
	ds_read_b128 v[8:11], v111 offset:49152
	ds_read_b128 v[12:15], v111 offset:57344
	s_waitcnt lgkmcnt(0)
	v_mfma_f32_16x16x32_f16 v[52:55], v[84:87], v[124:127], v[52:55]
	v_mfma_f32_16x16x32_f16 v[56:59], v[88:91], v[124:127], v[56:59]
	v_mfma_f32_16x16x32_f16 v[60:63], v[92:95], v[124:127], v[60:63]
	v_mfma_f32_16x16x32_f16 v[64:67], v[96:99], v[124:127], v[64:67]
	v_mfma_f32_16x16x32_f16 v[68:71], v[0:3], v[124:127], v[68:71]
	v_mfma_f32_16x16x32_f16 v[72:75], v[4:7], v[124:127], v[72:75]
	v_mfma_f32_16x16x32_f16 v[76:79], v[8:11], v[124:127], v[76:79]
	v_mfma_f32_16x16x32_f16 v[80:83], v[12:15], v[124:127], v[80:83]
	s_nop 7
	s_nop 3
	v_max_f32_e32 v52, 0, v52
	v_max_f32_e32 v53, 0, v53
	v_max_f32_e32 v54, 0, v54
	v_max_f32_e32 v55, 0, v55
	v_max_f32_e32 v56, 0, v56
	v_max_f32_e32 v57, 0, v57
	v_max_f32_e32 v58, 0, v58
	v_max_f32_e32 v59, 0, v59
	v_max_f32_e32 v60, 0, v60
	v_max_f32_e32 v61, 0, v61
	v_max_f32_e32 v62, 0, v62
	v_max_f32_e32 v63, 0, v63
	v_max_f32_e32 v64, 0, v64
	v_max_f32_e32 v65, 0, v65
	v_max_f32_e32 v66, 0, v66
	v_max_f32_e32 v67, 0, v67
	v_max_f32_e32 v68, 0, v68
	v_max_f32_e32 v69, 0, v69
	v_max_f32_e32 v70, 0, v70
	v_max_f32_e32 v71, 0, v71
	v_max_f32_e32 v72, 0, v72
	v_max_f32_e32 v73, 0, v73
	v_max_f32_e32 v74, 0, v74
	v_max_f32_e32 v75, 0, v75
	v_max_f32_e32 v76, 0, v76
	v_max_f32_e32 v77, 0, v77
	v_max_f32_e32 v78, 0, v78
	v_max_f32_e32 v79, 0, v79
	v_max_f32_e32 v80, 0, v80
	v_max_f32_e32 v81, 0, v81
	v_max_f32_e32 v82, 0, v82
	v_max_f32_e32 v83, 0, v83
	v_max3_f32 v1, v52, v53, v54
	v_max3_f32 v1, v1, v55, v56
	v_max3_f32 v1, v1, v57, v58
	v_max3_f32 v1, v1, v59, v60
	v_max3_f32 v1, v1, v61, v62
	v_max3_f32 v1, v1, v63, v64
	v_max3_f32 v1, v1, v65, v66
	v_max3_f32 v1, v1, v67, v68
	v_max3_f32 v1, v1, v69, v70
	v_max3_f32 v1, v1, v71, v72
	v_max3_f32 v1, v1, v73, v74
	v_max3_f32 v1, v1, v75, v76
	v_max3_f32 v1, v1, v77, v78
	v_max3_f32 v1, v1, v79, v80
	v_max3_f32 v1, v1, v81, v82
	v_max_f32_e32 v1, v1, v83
	v_lshl_or_b32 v0, v106, 4, v105
	v_xor_b32_e32 v2, 16, v0
	v_lshlrev_b32_e32 v2, 2, v2
	ds_bpermute_b32 v3, v2, v1
	s_waitcnt lgkmcnt(0)
	v_max_f32_e32 v1, v1, v3
	v_xor_b32_e32 v2, 32, v0
	v_lshlrev_b32_e32 v2, 2, v2
	ds_bpermute_b32 v3, v2, v1
	s_waitcnt lgkmcnt(0)
	v_max_f32_e32 v1, v1, v3
	s_mov_b32 s58, 0x437f0000
	v_div_scale_f32 v5, s[62:63], v1, v1, s58
	v_rcp_f32_e32 v6, v5
	v_div_scale_f32 v7, vcc, s58, v1, s58
	v_fma_f32 v8, -v5, v6, 1.0
	v_fmac_f32_e32 v6, v8, v6
	v_mul_f32_e32 v8, v7, v6
	v_fma_f32 v4, -v5, v8, v7
	v_fmac_f32_e32 v8, v4, v6
	v_fma_f32 v5, -v5, v8, v7
	v_div_fmas_f32 v5, v5, v6, v8
	v_div_fixup_f32 v4, v5, v1, s58
	v_cmp_lt_f32_e32 vcc, 0, v1
	s_nop 1
	v_cndmask_b32_e32 v4, 0, v4, vcc
	v_mul_u32_u24_e32 v9, 0x110, v105
	v_lshl_add_u32 v9, v106, 3, v9
	v_add_u32_e32 v9, s48, v9
	v_mul_u32_u24_e32 v10, 0x110, v106
	v_lshl_add_u32 v10, v105, 4, v10
	v_add_u32_e32 v10, s48, v10
	v_mul_u32_u24_e32 v11, 0x90, v105
	v_lshl_add_u32 v11, v106, 2, v11
	v_add_u32_e32 v11, s48, v11
	v_lshrrev_b32_e32 v14, 3, v0
	v_and_b32_e32 v16, 7, v0
	v_mul_u32_u24_e32 v12, 0x90, v14
	v_lshl_add_u32 v12, v16, 4, v12
	v_add_u32_e32 v12, s48, v12
	v_lshlrev_b32_e32 v14, 2, v14
	v_lshlrev_b32_e32 v16, 4, v16
	v_lshlrev_b32_e32 v13, 2, v106
	v_lshlrev_b32_e32 v15, 4, v105
	ds_bpermute_b32 v20, v13, v104 offset:0
	ds_bpermute_b32 v21, v13, v104 offset:16
	ds_bpermute_b32 v22, v13, v104 offset:32
	ds_bpermute_b32 v23, v13, v104 offset:48
	ds_bpermute_b32 v24, v14, v104 offset:0
	ds_bpermute_b32 v25, v14, v104 offset:32
	s_waitcnt lgkmcnt(0)
	v_cvt_pk_f16_f32 v26, v52, v53
	v_cvt_pk_f16_f32 v27, v54, v55
	ds_write_b64 v9, v[26:27] offset:0
	v_cvt_pk_f16_f32 v26, v56, v57
	v_cvt_pk_f16_f32 v27, v58, v59
	ds_write_b64 v9, v[26:27] offset:32
	v_cvt_pk_f16_f32 v26, v60, v61
	v_cvt_pk_f16_f32 v27, v62, v63
	ds_write_b64 v9, v[26:27] offset:64
	v_cvt_pk_f16_f32 v26, v64, v65
	v_cvt_pk_f16_f32 v27, v66, v67
	ds_write_b64 v9, v[26:27] offset:96
	v_cvt_pk_f16_f32 v26, v68, v69
	v_cvt_pk_f16_f32 v27, v70, v71
	ds_write_b64 v9, v[26:27] offset:128
	v_cvt_pk_f16_f32 v26, v72, v73
	v_cvt_pk_f16_f32 v27, v74, v75
	ds_write_b64 v9, v[26:27] offset:160
	v_cvt_pk_f16_f32 v26, v76, v77
	v_cvt_pk_f16_f32 v27, v78, v79
	ds_write_b64 v9, v[26:27] offset:192
	v_cvt_pk_f16_f32 v26, v80, v81
	v_cvt_pk_f16_f32 v27, v82, v83
	ds_write_b64 v9, v[26:27] offset:224
	ds_read_b128 v[28:31], v10 offset:0
	ds_read_b128 v[32:35], v10 offset:1088
	ds_read_b128 v[36:39], v10 offset:2176
	ds_read_b128 v[40:43], v10 offset:3264
	s_waitcnt lgkmcnt(3)
	v_lshl_or_b32 v20, v20, 8, v15
	global_store_dwordx4 v20, v[28:31], s[26:27] sc1
	s_waitcnt lgkmcnt(2)
	v_lshl_or_b32 v21, v21, 8, v15
	global_store_dwordx4 v21, v[32:35], s[26:27] sc1
	s_waitcnt lgkmcnt(1)
	v_lshl_or_b32 v22, v22, 8, v15
	global_store_dwordx4 v22, v[36:39], s[26:27] sc1
	s_waitcnt lgkmcnt(0)
	v_lshl_or_b32 v23, v23, 8, v15
	global_store_dwordx4 v23, v[40:43], s[26:27] sc1
	v_mul_f32_e32 v44, v4, v52
	v_mul_f32_e32 v45, v4, v53
	v_mul_f32_e32 v46, v4, v54
	v_mul_f32_e32 v47, v4, v55
	v_rndne_f32_e32 v44, v44
	v_rndne_f32_e32 v45, v45
	v_rndne_f32_e32 v46, v46
	v_rndne_f32_e32 v47, v47
	v_cvt_i32_f32_e32 v44, v44
	v_cvt_i32_f32_e32 v45, v45
	v_cvt_i32_f32_e32 v46, v46
	v_cvt_i32_f32_e32 v47, v47
	v_lshl_or_b32 v44, v45, 8, v44
	v_lshl_or_b32 v44, v46, 16, v44
	v_lshl_or_b32 v44, v47, 24, v44
	ds_write_b32 v11, v44 offset:0
	v_mul_f32_e32 v44, v4, v56
	v_mul_f32_e32 v45, v4, v57
	v_mul_f32_e32 v46, v4, v58
	v_mul_f32_e32 v47, v4, v59
	v_rndne_f32_e32 v44, v44
	v_rndne_f32_e32 v45, v45
	v_rndne_f32_e32 v46, v46
	v_rndne_f32_e32 v47, v47
	v_cvt_i32_f32_e32 v44, v44
	v_cvt_i32_f32_e32 v45, v45
	v_cvt_i32_f32_e32 v46, v46
	v_cvt_i32_f32_e32 v47, v47
	v_lshl_or_b32 v44, v45, 8, v44
	v_lshl_or_b32 v44, v46, 16, v44
	v_lshl_or_b32 v44, v47, 24, v44
	ds_write_b32 v11, v44 offset:16
	v_mul_f32_e32 v44, v4, v60
	v_mul_f32_e32 v45, v4, v61
	v_mul_f32_e32 v46, v4, v62
	v_mul_f32_e32 v47, v4, v63
	v_rndne_f32_e32 v44, v44
	v_rndne_f32_e32 v45, v45
	v_rndne_f32_e32 v46, v46
	v_rndne_f32_e32 v47, v47
	v_cvt_i32_f32_e32 v44, v44
	v_cvt_i32_f32_e32 v45, v45
	v_cvt_i32_f32_e32 v46, v46
	v_cvt_i32_f32_e32 v47, v47
	v_lshl_or_b32 v44, v45, 8, v44
	v_lshl_or_b32 v44, v46, 16, v44
	v_lshl_or_b32 v44, v47, 24, v44
	ds_write_b32 v11, v44 offset:32
	v_mul_f32_e32 v44, v4, v64
	v_mul_f32_e32 v45, v4, v65
	v_mul_f32_e32 v46, v4, v66
	v_mul_f32_e32 v47, v4, v67
	v_rndne_f32_e32 v44, v44
	v_rndne_f32_e32 v45, v45
	v_rndne_f32_e32 v46, v46
	v_rndne_f32_e32 v47, v47
	v_cvt_i32_f32_e32 v44, v44
	v_cvt_i32_f32_e32 v45, v45
	v_cvt_i32_f32_e32 v46, v46
	v_cvt_i32_f32_e32 v47, v47
	v_lshl_or_b32 v44, v45, 8, v44
	v_lshl_or_b32 v44, v46, 16, v44
	v_lshl_or_b32 v44, v47, 24, v44
	ds_write_b32 v11, v44 offset:48
	v_mul_f32_e32 v44, v4, v68
	v_mul_f32_e32 v45, v4, v69
	v_mul_f32_e32 v46, v4, v70
	v_mul_f32_e32 v47, v4, v71
	v_rndne_f32_e32 v44, v44
	v_rndne_f32_e32 v45, v45
	v_rndne_f32_e32 v46, v46
	v_rndne_f32_e32 v47, v47
	v_cvt_i32_f32_e32 v44, v44
	v_cvt_i32_f32_e32 v45, v45
	v_cvt_i32_f32_e32 v46, v46
	v_cvt_i32_f32_e32 v47, v47
	v_lshl_or_b32 v44, v45, 8, v44
	v_lshl_or_b32 v44, v46, 16, v44
	v_lshl_or_b32 v44, v47, 24, v44
	ds_write_b32 v11, v44 offset:64
	v_mul_f32_e32 v44, v4, v72
	v_mul_f32_e32 v45, v4, v73
	v_mul_f32_e32 v46, v4, v74
	v_mul_f32_e32 v47, v4, v75
	v_rndne_f32_e32 v44, v44
	v_rndne_f32_e32 v45, v45
	v_rndne_f32_e32 v46, v46
	v_rndne_f32_e32 v47, v47
	v_cvt_i32_f32_e32 v44, v44
	v_cvt_i32_f32_e32 v45, v45
	v_cvt_i32_f32_e32 v46, v46
	v_cvt_i32_f32_e32 v47, v47
	v_lshl_or_b32 v44, v45, 8, v44
	v_lshl_or_b32 v44, v46, 16, v44
	v_lshl_or_b32 v44, v47, 24, v44
	ds_write_b32 v11, v44 offset:80
	v_mul_f32_e32 v44, v4, v76
	v_mul_f32_e32 v45, v4, v77
	v_mul_f32_e32 v46, v4, v78
	v_mul_f32_e32 v47, v4, v79
	v_rndne_f32_e32 v44, v44
	v_rndne_f32_e32 v45, v45
	v_rndne_f32_e32 v46, v46
	v_rndne_f32_e32 v47, v47
	v_cvt_i32_f32_e32 v44, v44
	v_cvt_i32_f32_e32 v45, v45
	v_cvt_i32_f32_e32 v46, v46
	v_cvt_i32_f32_e32 v47, v47
	v_lshl_or_b32 v44, v45, 8, v44
	v_lshl_or_b32 v44, v46, 16, v44
	v_lshl_or_b32 v44, v47, 24, v44
	ds_write_b32 v11, v44 offset:96
	v_mul_f32_e32 v44, v4, v80
	v_mul_f32_e32 v45, v4, v81
	v_mul_f32_e32 v46, v4, v82
	v_mul_f32_e32 v47, v4, v83
	v_rndne_f32_e32 v44, v44
	v_rndne_f32_e32 v45, v45
	v_rndne_f32_e32 v46, v46
	v_rndne_f32_e32 v47, v47
	v_cvt_i32_f32_e32 v44, v44
	v_cvt_i32_f32_e32 v45, v45
	v_cvt_i32_f32_e32 v46, v46
	v_cvt_i32_f32_e32 v47, v47
	v_lshl_or_b32 v44, v45, 8, v44
	v_lshl_or_b32 v44, v46, 16, v44
	v_lshl_or_b32 v44, v47, 24, v44
	ds_write_b32 v11, v44 offset:112
	ds_read_b128 v[84:87], v12 offset:0
	ds_read_b128 v[88:91], v12 offset:1152
	s_waitcnt lgkmcnt(1)
	v_lshl_or_b32 v24, v24, 7, v16
	global_store_dwordx4 v24, v[84:87], s[28:29] sc1
	s_waitcnt lgkmcnt(0)
	v_lshl_or_b32 v25, v25, 7, v16
	global_store_dwordx4 v25, v[88:91], s[28:29] sc1
	v_cmp_eq_u32_e32 vcc, 0, v106
	s_and_saveexec_b64 s[44:45], vcc
	s_mov_b32 s58, 0x3b808081
	v_fma_mixlo_f16 v2, v1, s58, 0
	v_lshlrev_b32_e32 v3, 1, v104
	global_store_short v3, v2, s[30:31]
	s_endpgm
	.p2alignl 8, 3212836864

.Lg2_sel_done:
	s_min_i32 s40, s41, 32
	s_add_i32 s40, s40, 3
	s_and_b32 s40, s40, 0x3c
	s_max_i32 s40, s40, 4
	v_mov_b32_e32 v2, 0
	v_mov_b32_e32 v3, 0
	v_mov_b32_e32 v4, 0
	v_mov_b32_e32 v5, 0
	v_mov_b32_e32 v6, 0
	v_mov_b32_e32 v7, 0
	v_mov_b32_e32 v8, 0
	v_mov_b32_e32 v9, 0
	v_mov_b32_e32 v10, 0
	v_mov_b32_e32 v11, 0
	v_mov_b32_e32 v12, 0
	v_mov_b32_e32 v13, 0
	v_mov_b32_e32 v14, 0
	v_mov_b32_e32 v15, 0
	v_mov_b32_e32 v16, 0
	v_mov_b32_e32 v17, 0
	s_waitcnt lgkmcnt(0)
	ds_bpermute_b32 v94, v90, v73 offset:0
	ds_bpermute_b32 v98, v90, v75 offset:0
	ds_bpermute_b32 v95, v90, v73 offset:4
	ds_bpermute_b32 v99, v90, v75 offset:4
	ds_bpermute_b32 v79, v90, v73 offset:8
	ds_bpermute_b32 v81, v90, v75 offset:8
	s_waitcnt lgkmcnt(2)
	v_and_b32_e32 v84, 0xffff, v94
	v_lshl_or_b32 v83, v84, 7, v89
	v_cmp_lt_i32_e32 vcc, 0, v78
	s_mov_b64 exec, vcc
	global_load_dwordx4 v[20:23], v83, s[12:13]
	s_mov_b64 exec, -1
	v_cvt_f32_f16_e32 v52, v98
	v_lshrrev_b32_e32 v84, 16, v94
	v_lshl_or_b32 v83, v84, 7, v89
	v_cmp_lt_i32_e32 vcc, 1, v78
	s_mov_b64 exec, vcc
	global_load_dwordx4 v[24:27], v83, s[12:13]
	s_mov_b64 exec, -1
	v_cvt_f32_f16_sdwa v53, v98 dst_sel:DWORD dst_unused:UNUSED_PAD src0_sel:WORD_1
	v_and_b32_e32 v84, 0xffff, v95
	v_lshl_or_b32 v83, v84, 7, v89
	v_cmp_lt_i32_e32 vcc, 2, v78
	s_mov_b64 exec, vcc
	global_load_dwordx4 v[28:31], v83, s[12:13]
	s_mov_b64 exec, -1
	v_cvt_f32_f16_e32 v54, v99
	v_lshrrev_b32_e32 v84, 16, v95
	v_lshl_or_b32 v83, v84, 7, v89
	v_cmp_lt_i32_e32 vcc, 3, v78
	s_mov_b64 exec, vcc
	global_load_dwordx4 v[32:35], v83, s[12:13]
	s_mov_b64 exec, -1
	v_cvt_f32_f16_sdwa v55, v99 dst_sel:DWORD dst_unused:UNUSED_PAD src0_sel:WORD_1
	s_cmp_le_u32 s40, 4
	s_cbranch_scc1 .Lg2_tail0
	s_waitcnt lgkmcnt(0)
	ds_bpermute_b32 v80, v90, v73 offset:12
	ds_bpermute_b32 v82, v90, v75 offset:12
	s_waitcnt vmcnt(3)
	v_cvt_f32_ubyte0_e32 v85, v20
	v_cvt_f32_ubyte1_e32 v86, v20
	v_cvt_f32_ubyte2_e32 v87, v20
	v_cvt_f32_ubyte3_e32 v88, v20
	v_fmac_f32_e32 v2, v85, v52
	v_fmac_f32_e32 v3, v86, v52
	v_fmac_f32_e32 v4, v87, v52
	v_fmac_f32_e32 v5, v88, v52
	v_cvt_f32_ubyte0_e32 v85, v21
	v_cvt_f32_ubyte1_e32 v86, v21
	v_cvt_f32_ubyte2_e32 v87, v21
	v_cvt_f32_ubyte3_e32 v88, v21
	v_fmac_f32_e32 v6, v85, v52
	v_fmac_f32_e32 v7, v86, v52
	v_fmac_f32_e32 v8, v87, v52
	v_fmac_f32_e32 v9, v88, v52
	v_cvt_f32_ubyte0_e32 v85, v22
	v_cvt_f32_ubyte1_e32 v86, v22
	v_cvt_f32_ubyte2_e32 v87, v22
	v_cvt_f32_ubyte3_e32 v88, v22
	v_fmac_f32_e32 v10, v85, v52
	v_fmac_f32_e32 v11, v86, v52
	v_fmac_f32_e32 v12, v87, v52
	v_fmac_f32_e32 v13, v88, v52
	v_cvt_f32_ubyte0_e32 v85, v23
	v_cvt_f32_ubyte1_e32 v86, v23
	v_cvt_f32_ubyte2_e32 v87, v23
	v_cvt_f32_ubyte3_e32 v88, v23
	v_fmac_f32_e32 v14, v85, v52
	v_fmac_f32_e32 v15, v86, v52
	v_fmac_f32_e32 v16, v87, v52
	v_fmac_f32_e32 v17, v88, v52
	v_and_b32_e32 v84, 0xffff, v79
	v_lshl_or_b32 v83, v84, 7, v89
	v_cmp_lt_i32_e32 vcc, 4, v78
	s_mov_b64 exec, vcc
	global_load_dwordx4 v[20:23], v83, s[12:13]
	s_mov_b64 exec, -1
	v_cvt_f32_f16_e32 v52, v81
	s_waitcnt vmcnt(3)
	v_cvt_f32_ubyte0_e32 v85, v24
	v_cvt_f32_ubyte1_e32 v86, v24
	v_cvt_f32_ubyte2_e32 v87, v24
	v_cvt_f32_ubyte3_e32 v88, v24
	v_fmac_f32_e32 v2, v85, v53
	v_fmac_f32_e32 v3, v86, v53
	v_fmac_f32_e32 v4, v87, v53
	v_fmac_f32_e32 v5, v88, v53
	v_cvt_f32_ubyte0_e32 v85, v25
	v_cvt_f32_ubyte1_e32 v86, v25
	v_cvt_f32_ubyte2_e32 v87, v25
	v_cvt_f32_ubyte3_e32 v88, v25
	v_fmac_f32_e32 v6, v85, v53
	v_fmac_f32_e32 v7, v86, v53
	v_fmac_f32_e32 v8, v87, v53
	v_fmac_f32_e32 v9, v88, v53
	v_cvt_f32_ubyte0_e32 v85, v26
	v_cvt_f32_ubyte1_e32 v86, v26
	v_cvt_f32_ubyte2_e32 v87, v26
	v_cvt_f32_ubyte3_e32 v88, v26
	v_fmac_f32_e32 v10, v85, v53
	v_fmac_f32_e32 v11, v86, v53
	v_fmac_f32_e32 v12, v87, v53
	v_fmac_f32_e32 v13, v88, v53
	v_cvt_f32_ubyte0_e32 v85, v27
	v_cvt_f32_ubyte1_e32 v86, v27
	v_cvt_f32_ubyte2_e32 v87, v27
	v_cvt_f32_ubyte3_e32 v88, v27
	v_fmac_f32_e32 v14, v85, v53
	v_fmac_f32_e32 v15, v86, v53
	v_fmac_f32_e32 v16, v87, v53
	v_fmac_f32_e32 v17, v88, v53
	v_lshrrev_b32_e32 v84, 16, v79
	v_lshl_or_b32 v83, v84, 7, v89
	v_cmp_lt_i32_e32 vcc, 5, v78
	s_mov_b64 exec, vcc
	global_load_dwordx4 v[24:27], v83, s[12:13]
	s_mov_b64 exec, -1
	v_cvt_f32_f16_sdwa v53, v81 dst_sel:DWORD dst_unused:UNUSED_PAD src0_sel:WORD_1
	s_waitcnt lgkmcnt(0)
	ds_bpermute_b32 v79, v90, v73 offset:16
	ds_bpermute_b32 v81, v90, v75 offset:16
	s_waitcnt vmcnt(3)
	v_cvt_f32_ubyte0_e32 v85, v28
	v_cvt_f32_ubyte1_e32 v86, v28
	v_cvt_f32_ubyte2_e32 v87, v28
	v_cvt_f32_ubyte3_e32 v88, v28
	v_fmac_f32_e32 v2, v85, v54
	v_fmac_f32_e32 v3, v86, v54
	v_fmac_f32_e32 v4, v87, v54
	v_fmac_f32_e32 v5, v88, v54
	v_cvt_f32_ubyte0_e32 v85, v29
	v_cvt_f32_ubyte1_e32 v86, v29
	v_cvt_f32_ubyte2_e32 v87, v29
	v_cvt_f32_ubyte3_e32 v88, v29
	v_fmac_f32_e32 v6, v85, v54
	v_fmac_f32_e32 v7, v86, v54
	v_fmac_f32_e32 v8, v87, v54
	v_fmac_f32_e32 v9, v88, v54
	v_cvt_f32_ubyte0_e32 v85, v30
	v_cvt_f32_ubyte1_e32 v86, v30
	v_cvt_f32_ubyte2_e32 v87, v30
	v_cvt_f32_ubyte3_e32 v88, v30
	v_fmac_f32_e32 v10, v85, v54
	v_fmac_f32_e32 v11, v86, v54
	v_fmac_f32_e32 v12, v87, v54
	v_fmac_f32_e32 v13, v88, v54
	v_cvt_f32_ubyte0_e32 v85, v31
	v_cvt_f32_ubyte1_e32 v86, v31
	v_cvt_f32_ubyte2_e32 v87, v31
	v_cvt_f32_ubyte3_e32 v88, v31
	v_fmac_f32_e32 v14, v85, v54
	v_fmac_f32_e32 v15, v86, v54
	v_fmac_f32_e32 v16, v87, v54
	v_fmac_f32_e32 v17, v88, v54
	v_and_b32_e32 v84, 0xffff, v80
	v_lshl_or_b32 v83, v84, 7, v89
	v_cmp_lt_i32_e32 vcc, 6, v78
	s_mov_b64 exec, vcc
	global_load_dwordx4 v[28:31], v83, s[12:13]
	s_mov_b64 exec, -1
	v_cvt_f32_f16_e32 v54, v82
	s_waitcnt vmcnt(3)
	v_cvt_f32_ubyte0_e32 v85, v32
	v_cvt_f32_ubyte1_e32 v86, v32
	v_cvt_f32_ubyte2_e32 v87, v32
	v_cvt_f32_ubyte3_e32 v88, v32
	v_fmac_f32_e32 v2, v85, v55
	v_fmac_f32_e32 v3, v86, v55
	v_fmac_f32_e32 v4, v87, v55
	v_fmac_f32_e32 v5, v88, v55
	v_cvt_f32_ubyte0_e32 v85, v33
	v_cvt_f32_ubyte1_e32 v86, v33
	v_cvt_f32_ubyte2_e32 v87, v33
	v_cvt_f32_ubyte3_e32 v88, v33
	v_fmac_f32_e32 v6, v85, v55
	v_fmac_f32_e32 v7, v86, v55
	v_fmac_f32_e32 v8, v87, v55
	v_fmac_f32_e32 v9, v88, v55
	v_cvt_f32_ubyte0_e32 v85, v34
	v_cvt_f32_ubyte1_e32 v86, v34
	v_cvt_f32_ubyte2_e32 v87, v34
	v_cvt_f32_ubyte3_e32 v88, v34
	v_fmac_f32_e32 v10, v85, v55
	v_fmac_f32_e32 v11, v86, v55
	v_fmac_f32_e32 v12, v87, v55
	v_fmac_f32_e32 v13, v88, v55
	v_cvt_f32_ubyte0_e32 v85, v35
	v_cvt_f32_ubyte1_e32 v86, v35
	v_cvt_f32_ubyte2_e32 v87, v35
	v_cvt_f32_ubyte3_e32 v88, v35
	v_fmac_f32_e32 v14, v85, v55
	v_fmac_f32_e32 v15, v86, v55
	v_fmac_f32_e32 v16, v87, v55
	v_fmac_f32_e32 v17, v88, v55
	v_lshrrev_b32_e32 v84, 16, v80
	v_lshl_or_b32 v83, v84, 7, v89
	v_cmp_lt_i32_e32 vcc, 7, v78
	s_mov_b64 exec, vcc
	global_load_dwordx4 v[32:35], v83, s[12:13]
	s_mov_b64 exec, -1
	v_cvt_f32_f16_sdwa v55, v82 dst_sel:DWORD dst_unused:UNUSED_PAD src0_sel:WORD_1
	s_cmp_le_u32 s40, 8
	s_cbranch_scc1 .Lg2_tail0
	s_waitcnt lgkmcnt(0)
	ds_bpermute_b32 v80, v90, v73 offset:20
	ds_bpermute_b32 v82, v90, v75 offset:20
	s_waitcnt vmcnt(3)
	v_cvt_f32_ubyte0_e32 v85, v20
	v_cvt_f32_ubyte1_e32 v86, v20
	v_cvt_f32_ubyte2_e32 v87, v20
	v_cvt_f32_ubyte3_e32 v88, v20
	v_fmac_f32_e32 v2, v85, v52
	v_fmac_f32_e32 v3, v86, v52
	v_fmac_f32_e32 v4, v87, v52
	v_fmac_f32_e32 v5, v88, v52
	v_cvt_f32_ubyte0_e32 v85, v21
	v_cvt_f32_ubyte1_e32 v86, v21
	v_cvt_f32_ubyte2_e32 v87, v21
	v_cvt_f32_ubyte3_e32 v88, v21
	v_fmac_f32_e32 v6, v85, v52
	v_fmac_f32_e32 v7, v86, v52
	v_fmac_f32_e32 v8, v87, v52
	v_fmac_f32_e32 v9, v88, v52
	v_cvt_f32_ubyte0_e32 v85, v22
	v_cvt_f32_ubyte1_e32 v86, v22
	v_cvt_f32_ubyte2_e32 v87, v22
	v_cvt_f32_ubyte3_e32 v88, v22
	v_fmac_f32_e32 v10, v85, v52
	v_fmac_f32_e32 v11, v86, v52
	v_fmac_f32_e32 v12, v87, v52
	v_fmac_f32_e32 v13, v88, v52
	v_cvt_f32_ubyte0_e32 v85, v23
	v_cvt_f32_ubyte1_e32 v86, v23
	v_cvt_f32_ubyte2_e32 v87, v23
	v_cvt_f32_ubyte3_e32 v88, v23
	v_fmac_f32_e32 v14, v85, v52
	v_fmac_f32_e32 v15, v86, v52
	v_fmac_f32_e32 v16, v87, v52
	v_fmac_f32_e32 v17, v88, v52
	v_and_b32_e32 v84, 0xffff, v79
	v_lshl_or_b32 v83, v84, 7, v89
	v_cmp_lt_i32_e32 vcc, 8, v78
	s_mov_b64 exec, vcc
	global_load_dwordx4 v[20:23], v83, s[12:13]
	s_mov_b64 exec, -1
	v_cvt_f32_f16_e32 v52, v81
	s_waitcnt vmcnt(3)
	v_cvt_f32_ubyte0_e32 v85, v24
	v_cvt_f32_ubyte1_e32 v86, v24
	v_cvt_f32_ubyte2_e32 v87, v24
	v_cvt_f32_ubyte3_e32 v88, v24
	v_fmac_f32_e32 v2, v85, v53
	v_fmac_f32_e32 v3, v86, v53
	v_fmac_f32_e32 v4, v87, v53
	v_fmac_f32_e32 v5, v88, v53
	v_cvt_f32_ubyte0_e32 v85, v25
	v_cvt_f32_ubyte1_e32 v86, v25
	v_cvt_f32_ubyte2_e32 v87, v25
	v_cvt_f32_ubyte3_e32 v88, v25
	v_fmac_f32_e32 v6, v85, v53
	v_fmac_f32_e32 v7, v86, v53
	v_fmac_f32_e32 v8, v87, v53
	v_fmac_f32_e32 v9, v88, v53
	v_cvt_f32_ubyte0_e32 v85, v26
	v_cvt_f32_ubyte1_e32 v86, v26
	v_cvt_f32_ubyte2_e32 v87, v26
	v_cvt_f32_ubyte3_e32 v88, v26
	v_fmac_f32_e32 v10, v85, v53
	v_fmac_f32_e32 v11, v86, v53
	v_fmac_f32_e32 v12, v87, v53
	v_fmac_f32_e32 v13, v88, v53
	v_cvt_f32_ubyte0_e32 v85, v27
	v_cvt_f32_ubyte1_e32 v86, v27
	v_cvt_f32_ubyte2_e32 v87, v27
	v_cvt_f32_ubyte3_e32 v88, v27
	v_fmac_f32_e32 v14, v85, v53
	v_fmac_f32_e32 v15, v86, v53
	v_fmac_f32_e32 v16, v87, v53
	v_fmac_f32_e32 v17, v88, v53
	v_lshrrev_b32_e32 v84, 16, v79
	v_lshl_or_b32 v83, v84, 7, v89
	v_cmp_lt_i32_e32 vcc, 9, v78
	s_mov_b64 exec, vcc
	global_load_dwordx4 v[24:27], v83, s[12:13]
	s_mov_b64 exec, -1
	v_cvt_f32_f16_sdwa v53, v81 dst_sel:DWORD dst_unused:UNUSED_PAD src0_sel:WORD_1
	s_waitcnt lgkmcnt(0)
	ds_bpermute_b32 v79, v90, v73 offset:24
	ds_bpermute_b32 v81, v90, v75 offset:24
	s_waitcnt vmcnt(3)
	v_cvt_f32_ubyte0_e32 v85, v28
	v_cvt_f32_ubyte1_e32 v86, v28
	v_cvt_f32_ubyte2_e32 v87, v28
	v_cvt_f32_ubyte3_e32 v88, v28
	v_fmac_f32_e32 v2, v85, v54
	v_fmac_f32_e32 v3, v86, v54
	v_fmac_f32_e32 v4, v87, v54
	v_fmac_f32_e32 v5, v88, v54
	v_cvt_f32_ubyte0_e32 v85, v29
	v_cvt_f32_ubyte1_e32 v86, v29
	v_cvt_f32_ubyte2_e32 v87, v29
	v_cvt_f32_ubyte3_e32 v88, v29
	v_fmac_f32_e32 v6, v85, v54
	v_fmac_f32_e32 v7, v86, v54
	v_fmac_f32_e32 v8, v87, v54
	v_fmac_f32_e32 v9, v88, v54
	v_cvt_f32_ubyte0_e32 v85, v30
	v_cvt_f32_ubyte1_e32 v86, v30
	v_cvt_f32_ubyte2_e32 v87, v30
	v_cvt_f32_ubyte3_e32 v88, v30
	v_fmac_f32_e32 v10, v85, v54
	v_fmac_f32_e32 v11, v86, v54
	v_fmac_f32_e32 v12, v87, v54
	v_fmac_f32_e32 v13, v88, v54
	v_cvt_f32_ubyte0_e32 v85, v31
	v_cvt_f32_ubyte1_e32 v86, v31
	v_cvt_f32_ubyte2_e32 v87, v31
	v_cvt_f32_ubyte3_e32 v88, v31
	v_fmac_f32_e32 v14, v85, v54
	v_fmac_f32_e32 v15, v86, v54
	v_fmac_f32_e32 v16, v87, v54
	v_fmac_f32_e32 v17, v88, v54
	v_and_b32_e32 v84, 0xffff, v80
	v_lshl_or_b32 v83, v84, 7, v89
	v_cmp_lt_i32_e32 vcc, 10, v78
	s_mov_b64 exec, vcc
	global_load_dwordx4 v[28:31], v83, s[12:13]
	s_mov_b64 exec, -1
	v_cvt_f32_f16_e32 v54, v82
	s_waitcnt vmcnt(3)
	v_cvt_f32_ubyte0_e32 v85, v32
	v_cvt_f32_ubyte1_e32 v86, v32
	v_cvt_f32_ubyte2_e32 v87, v32
	v_cvt_f32_ubyte3_e32 v88, v32
	v_fmac_f32_e32 v2, v85, v55
	v_fmac_f32_e32 v3, v86, v55
	v_fmac_f32_e32 v4, v87, v55
	v_fmac_f32_e32 v5, v88, v55
	v_cvt_f32_ubyte0_e32 v85, v33
	v_cvt_f32_ubyte1_e32 v86, v33
	v_cvt_f32_ubyte2_e32 v87, v33
	v_cvt_f32_ubyte3_e32 v88, v33
	v_fmac_f32_e32 v6, v85, v55
	v_fmac_f32_e32 v7, v86, v55
	v_fmac_f32_e32 v8, v87, v55
	v_fmac_f32_e32 v9, v88, v55
	v_cvt_f32_ubyte0_e32 v85, v34
	v_cvt_f32_ubyte1_e32 v86, v34
	v_cvt_f32_ubyte2_e32 v87, v34
	v_cvt_f32_ubyte3_e32 v88, v34
	v_fmac_f32_e32 v10, v85, v55
	v_fmac_f32_e32 v11, v86, v55
	v_fmac_f32_e32 v12, v87, v55
	v_fmac_f32_e32 v13, v88, v55
	v_cvt_f32_ubyte0_e32 v85, v35
	v_cvt_f32_ubyte1_e32 v86, v35
	v_cvt_f32_ubyte2_e32 v87, v35
	v_cvt_f32_ubyte3_e32 v88, v35
	v_fmac_f32_e32 v14, v85, v55
	v_fmac_f32_e32 v15, v86, v55
	v_fmac_f32_e32 v16, v87, v55
	v_fmac_f32_e32 v17, v88, v55
	v_lshrrev_b32_e32 v84, 16, v80
	v_lshl_or_b32 v83, v84, 7, v89
	v_cmp_lt_i32_e32 vcc, 11, v78
	s_mov_b64 exec, vcc
	global_load_dwordx4 v[32:35], v83, s[12:13]
	s_mov_b64 exec, -1
	v_cvt_f32_f16_sdwa v55, v82 dst_sel:DWORD dst_unused:UNUSED_PAD src0_sel:WORD_1
	s_cmp_le_u32 s40, 12
	s_cbranch_scc1 .Lg2_tail0
	s_waitcnt lgkmcnt(0)
	ds_bpermute_b32 v80, v90, v73 offset:28
	ds_bpermute_b32 v82, v90, v75 offset:28
	s_waitcnt vmcnt(3)
	v_cvt_f32_ubyte0_e32 v85, v20
	v_cvt_f32_ubyte1_e32 v86, v20
	v_cvt_f32_ubyte2_e32 v87, v20
	v_cvt_f32_ubyte3_e32 v88, v20
	v_fmac_f32_e32 v2, v85, v52
	v_fmac_f32_e32 v3, v86, v52
	v_fmac_f32_e32 v4, v87, v52
	v_fmac_f32_e32 v5, v88, v52
	v_cvt_f32_ubyte0_e32 v85, v21
	v_cvt_f32_ubyte1_e32 v86, v21
	v_cvt_f32_ubyte2_e32 v87, v21
	v_cvt_f32_ubyte3_e32 v88, v21
	v_fmac_f32_e32 v6, v85, v52
	v_fmac_f32_e32 v7, v86, v52
	v_fmac_f32_e32 v8, v87, v52
	v_fmac_f32_e32 v9, v88, v52
	v_cvt_f32_ubyte0_e32 v85, v22
	v_cvt_f32_ubyte1_e32 v86, v22
	v_cvt_f32_ubyte2_e32 v87, v22
	v_cvt_f32_ubyte3_e32 v88, v22
	v_fmac_f32_e32 v10, v85, v52
	v_fmac_f32_e32 v11, v86, v52
	v_fmac_f32_e32 v12, v87, v52
	v_fmac_f32_e32 v13, v88, v52
	v_cvt_f32_ubyte0_e32 v85, v23
	v_cvt_f32_ubyte1_e32 v86, v23
	v_cvt_f32_ubyte2_e32 v87, v23
	v_cvt_f32_ubyte3_e32 v88, v23
	v_fmac_f32_e32 v14, v85, v52
	v_fmac_f32_e32 v15, v86, v52
	v_fmac_f32_e32 v16, v87, v52
	v_fmac_f32_e32 v17, v88, v52
	v_and_b32_e32 v84, 0xffff, v79
	v_lshl_or_b32 v83, v84, 7, v89
	v_cmp_lt_i32_e32 vcc, 12, v78
	s_mov_b64 exec, vcc
	global_load_dwordx4 v[20:23], v83, s[12:13]
	s_mov_b64 exec, -1
	v_cvt_f32_f16_e32 v52, v81
	s_waitcnt vmcnt(3)
	v_cvt_f32_ubyte0_e32 v85, v24
	v_cvt_f32_ubyte1_e32 v86, v24
	v_cvt_f32_ubyte2_e32 v87, v24
	v_cvt_f32_ubyte3_e32 v88, v24
	v_fmac_f32_e32 v2, v85, v53
	v_fmac_f32_e32 v3, v86, v53
	v_fmac_f32_e32 v4, v87, v53
	v_fmac_f32_e32 v5, v88, v53
	v_cvt_f32_ubyte0_e32 v85, v25
	v_cvt_f32_ubyte1_e32 v86, v25
	v_cvt_f32_ubyte2_e32 v87, v25
	v_cvt_f32_ubyte3_e32 v88, v25
	v_fmac_f32_e32 v6, v85, v53
	v_fmac_f32_e32 v7, v86, v53
	v_fmac_f32_e32 v8, v87, v53
	v_fmac_f32_e32 v9, v88, v53
	v_cvt_f32_ubyte0_e32 v85, v26
	v_cvt_f32_ubyte1_e32 v86, v26
	v_cvt_f32_ubyte2_e32 v87, v26
	v_cvt_f32_ubyte3_e32 v88, v26
	v_fmac_f32_e32 v10, v85, v53
	v_fmac_f32_e32 v11, v86, v53
	v_fmac_f32_e32 v12, v87, v53
	v_fmac_f32_e32 v13, v88, v53
	v_cvt_f32_ubyte0_e32 v85, v27
	v_cvt_f32_ubyte1_e32 v86, v27
	v_cvt_f32_ubyte2_e32 v87, v27
	v_cvt_f32_ubyte3_e32 v88, v27
	v_fmac_f32_e32 v14, v85, v53
	v_fmac_f32_e32 v15, v86, v53
	v_fmac_f32_e32 v16, v87, v53
	v_fmac_f32_e32 v17, v88, v53
	v_lshrrev_b32_e32 v84, 16, v79
	v_lshl_or_b32 v83, v84, 7, v89
	v_cmp_lt_i32_e32 vcc, 13, v78
	s_mov_b64 exec, vcc
	global_load_dwordx4 v[24:27], v83, s[12:13]
	s_mov_b64 exec, -1
	v_cvt_f32_f16_sdwa v53, v81 dst_sel:DWORD dst_unused:UNUSED_PAD src0_sel:WORD_1
	s_waitcnt lgkmcnt(0)
	ds_bpermute_b32 v79, v90, v74 offset:0
	ds_bpermute_b32 v81, v90, v76 offset:0
	s_waitcnt vmcnt(3)
	v_cvt_f32_ubyte0_e32 v85, v28
	v_cvt_f32_ubyte1_e32 v86, v28
	v_cvt_f32_ubyte2_e32 v87, v28
	v_cvt_f32_ubyte3_e32 v88, v28
	v_fmac_f32_e32 v2, v85, v54
	v_fmac_f32_e32 v3, v86, v54
	v_fmac_f32_e32 v4, v87, v54
	v_fmac_f32_e32 v5, v88, v54
	v_cvt_f32_ubyte0_e32 v85, v29
	v_cvt_f32_ubyte1_e32 v86, v29
	v_cvt_f32_ubyte2_e32 v87, v29
	v_cvt_f32_ubyte3_e32 v88, v29
	v_fmac_f32_e32 v6, v85, v54
	v_fmac_f32_e32 v7, v86, v54
	v_fmac_f32_e32 v8, v87, v54
	v_fmac_f32_e32 v9, v88, v54
	v_cvt_f32_ubyte0_e32 v85, v30
	v_cvt_f32_ubyte1_e32 v86, v30
	v_cvt_f32_ubyte2_e32 v87, v30
	v_cvt_f32_ubyte3_e32 v88, v30
	v_fmac_f32_e32 v10, v85, v54
	v_fmac_f32_e32 v11, v86, v54
	v_fmac_f32_e32 v12, v87, v54
	v_fmac_f32_e32 v13, v88, v54
	v_cvt_f32_ubyte0_e32 v85, v31
	v_cvt_f32_ubyte1_e32 v86, v31
	v_cvt_f32_ubyte2_e32 v87, v31
	v_cvt_f32_ubyte3_e32 v88, v31
	v_fmac_f32_e32 v14, v85, v54
	v_fmac_f32_e32 v15, v86, v54
	v_fmac_f32_e32 v16, v87, v54
	v_fmac_f32_e32 v17, v88, v54
	v_and_b32_e32 v84, 0xffff, v80
	v_lshl_or_b32 v83, v84, 7, v89
	v_cmp_lt_i32_e32 vcc, 14, v78
	s_mov_b64 exec, vcc
	global_load_dwordx4 v[28:31], v83, s[12:13]
	s_mov_b64 exec, -1
	v_cvt_f32_f16_e32 v54, v82
	s_waitcnt vmcnt(3)
	v_cvt_f32_ubyte0_e32 v85, v32
	v_cvt_f32_ubyte1_e32 v86, v32
	v_cvt_f32_ubyte2_e32 v87, v32
	v_cvt_f32_ubyte3_e32 v88, v32
	v_fmac_f32_e32 v2, v85, v55
	v_fmac_f32_e32 v3, v86, v55
	v_fmac_f32_e32 v4, v87, v55
	v_fmac_f32_e32 v5, v88, v55
	v_cvt_f32_ubyte0_e32 v85, v33
	v_cvt_f32_ubyte1_e32 v86, v33
	v_cvt_f32_ubyte2_e32 v87, v33
	v_cvt_f32_ubyte3_e32 v88, v33
	v_fmac_f32_e32 v6, v85, v55
	v_fmac_f32_e32 v7, v86, v55
	v_fmac_f32_e32 v8, v87, v55
	v_fmac_f32_e32 v9, v88, v55
	v_cvt_f32_ubyte0_e32 v85, v34
	v_cvt_f32_ubyte1_e32 v86, v34
	v_cvt_f32_ubyte2_e32 v87, v34
	v_cvt_f32_ubyte3_e32 v88, v34
	v_fmac_f32_e32 v10, v85, v55
	v_fmac_f32_e32 v11, v86, v55
	v_fmac_f32_e32 v12, v87, v55
	v_fmac_f32_e32 v13, v88, v55
	v_cvt_f32_ubyte0_e32 v85, v35
	v_cvt_f32_ubyte1_e32 v86, v35
	v_cvt_f32_ubyte2_e32 v87, v35
	v_cvt_f32_ubyte3_e32 v88, v35
	v_fmac_f32_e32 v14, v85, v55
	v_fmac_f32_e32 v15, v86, v55
	v_fmac_f32_e32 v16, v87, v55
	v_fmac_f32_e32 v17, v88, v55
	v_lshrrev_b32_e32 v84, 16, v80
	v_lshl_or_b32 v83, v84, 7, v89
	v_cmp_lt_i32_e32 vcc, 15, v78
	s_mov_b64 exec, vcc
	global_load_dwordx4 v[32:35], v83, s[12:13]
	s_mov_b64 exec, -1
	v_cvt_f32_f16_sdwa v55, v82 dst_sel:DWORD dst_unused:UNUSED_PAD src0_sel:WORD_1
	s_cmp_le_u32 s40, 16
	s_cbranch_scc1 .Lg2_tail0
	s_waitcnt lgkmcnt(0)
	ds_bpermute_b32 v80, v90, v74 offset:4
	ds_bpermute_b32 v82, v90, v76 offset:4
	s_waitcnt vmcnt(3)
	v_cvt_f32_ubyte0_e32 v85, v20
	v_cvt_f32_ubyte1_e32 v86, v20
	v_cvt_f32_ubyte2_e32 v87, v20
	v_cvt_f32_ubyte3_e32 v88, v20
	v_fmac_f32_e32 v2, v85, v52
	v_fmac_f32_e32 v3, v86, v52
	v_fmac_f32_e32 v4, v87, v52
	v_fmac_f32_e32 v5, v88, v52
	v_cvt_f32_ubyte0_e32 v85, v21
	v_cvt_f32_ubyte1_e32 v86, v21
	v_cvt_f32_ubyte2_e32 v87, v21
	v_cvt_f32_ubyte3_e32 v88, v21
	v_fmac_f32_e32 v6, v85, v52
	v_fmac_f32_e32 v7, v86, v52
	v_fmac_f32_e32 v8, v87, v52
	v_fmac_f32_e32 v9, v88, v52
	v_cvt_f32_ubyte0_e32 v85, v22
	v_cvt_f32_ubyte1_e32 v86, v22
	v_cvt_f32_ubyte2_e32 v87, v22
	v_cvt_f32_ubyte3_e32 v88, v22
	v_fmac_f32_e32 v10, v85, v52
	v_fmac_f32_e32 v11, v86, v52
	v_fmac_f32_e32 v12, v87, v52
	v_fmac_f32_e32 v13, v88, v52
	v_cvt_f32_ubyte0_e32 v85, v23
	v_cvt_f32_ubyte1_e32 v86, v23
	v_cvt_f32_ubyte2_e32 v87, v23
	v_cvt_f32_ubyte3_e32 v88, v23
	v_fmac_f32_e32 v14, v85, v52
	v_fmac_f32_e32 v15, v86, v52
	v_fmac_f32_e32 v16, v87, v52
	v_fmac_f32_e32 v17, v88, v52
	v_and_b32_e32 v84, 0xffff, v79
	v_lshl_or_b32 v83, v84, 7, v89
	v_cmp_lt_i32_e32 vcc, 16, v78
	s_mov_b64 exec, vcc
	global_load_dwordx4 v[20:23], v83, s[12:13]
	s_mov_b64 exec, -1
	v_cvt_f32_f16_e32 v52, v81
	s_waitcnt vmcnt(3)
	v_cvt_f32_ubyte0_e32 v85, v24
	v_cvt_f32_ubyte1_e32 v86, v24
	v_cvt_f32_ubyte2_e32 v87, v24
	v_cvt_f32_ubyte3_e32 v88, v24
	v_fmac_f32_e32 v2, v85, v53
	v_fmac_f32_e32 v3, v86, v53
	v_fmac_f32_e32 v4, v87, v53
	v_fmac_f32_e32 v5, v88, v53
	v_cvt_f32_ubyte0_e32 v85, v25
	v_cvt_f32_ubyte1_e32 v86, v25
	v_cvt_f32_ubyte2_e32 v87, v25
	v_cvt_f32_ubyte3_e32 v88, v25
	v_fmac_f32_e32 v6, v85, v53
	v_fmac_f32_e32 v7, v86, v53
	v_fmac_f32_e32 v8, v87, v53
	v_fmac_f32_e32 v9, v88, v53
	v_cvt_f32_ubyte0_e32 v85, v26
	v_cvt_f32_ubyte1_e32 v86, v26
	v_cvt_f32_ubyte2_e32 v87, v26
	v_cvt_f32_ubyte3_e32 v88, v26
	v_fmac_f32_e32 v10, v85, v53
	v_fmac_f32_e32 v11, v86, v53
	v_fmac_f32_e32 v12, v87, v53
	v_fmac_f32_e32 v13, v88, v53
	v_cvt_f32_ubyte0_e32 v85, v27
	v_cvt_f32_ubyte1_e32 v86, v27
	v_cvt_f32_ubyte2_e32 v87, v27
	v_cvt_f32_ubyte3_e32 v88, v27
	v_fmac_f32_e32 v14, v85, v53
	v_fmac_f32_e32 v15, v86, v53
	v_fmac_f32_e32 v16, v87, v53
	v_fmac_f32_e32 v17, v88, v53
	v_lshrrev_b32_e32 v84, 16, v79
	v_lshl_or_b32 v83, v84, 7, v89
	v_cmp_lt_i32_e32 vcc, 17, v78
	s_mov_b64 exec, vcc
	global_load_dwordx4 v[24:27], v83, s[12:13]
	s_mov_b64 exec, -1
	v_cvt_f32_f16_sdwa v53, v81 dst_sel:DWORD dst_unused:UNUSED_PAD src0_sel:WORD_1
	s_waitcnt lgkmcnt(0)
	ds_bpermute_b32 v79, v90, v74 offset:8
	ds_bpermute_b32 v81, v90, v76 offset:8
	s_waitcnt vmcnt(3)
	v_cvt_f32_ubyte0_e32 v85, v28
	v_cvt_f32_ubyte1_e32 v86, v28
	v_cvt_f32_ubyte2_e32 v87, v28
	v_cvt_f32_ubyte3_e32 v88, v28
	v_fmac_f32_e32 v2, v85, v54
	v_fmac_f32_e32 v3, v86, v54
	v_fmac_f32_e32 v4, v87, v54
	v_fmac_f32_e32 v5, v88, v54
	v_cvt_f32_ubyte0_e32 v85, v29
	v_cvt_f32_ubyte1_e32 v86, v29
	v_cvt_f32_ubyte2_e32 v87, v29
	v_cvt_f32_ubyte3_e32 v88, v29
	v_fmac_f32_e32 v6, v85, v54
	v_fmac_f32_e32 v7, v86, v54
	v_fmac_f32_e32 v8, v87, v54
	v_fmac_f32_e32 v9, v88, v54
	v_cvt_f32_ubyte0_e32 v85, v30
	v_cvt_f32_ubyte1_e32 v86, v30
	v_cvt_f32_ubyte2_e32 v87, v30
	v_cvt_f32_ubyte3_e32 v88, v30
	v_fmac_f32_e32 v10, v85, v54
	v_fmac_f32_e32 v11, v86, v54
	v_fmac_f32_e32 v12, v87, v54
	v_fmac_f32_e32 v13, v88, v54
	v_cvt_f32_ubyte0_e32 v85, v31
	v_cvt_f32_ubyte1_e32 v86, v31
	v_cvt_f32_ubyte2_e32 v87, v31
	v_cvt_f32_ubyte3_e32 v88, v31
	v_fmac_f32_e32 v14, v85, v54
	v_fmac_f32_e32 v15, v86, v54
	v_fmac_f32_e32 v16, v87, v54
	v_fmac_f32_e32 v17, v88, v54
	v_and_b32_e32 v84, 0xffff, v80
	v_lshl_or_b32 v83, v84, 7, v89
	v_cmp_lt_i32_e32 vcc, 18, v78
	s_mov_b64 exec, vcc
	global_load_dwordx4 v[28:31], v83, s[12:13]
	s_mov_b64 exec, -1
	v_cvt_f32_f16_e32 v54, v82
	s_waitcnt vmcnt(3)
	v_cvt_f32_ubyte0_e32 v85, v32
	v_cvt_f32_ubyte1_e32 v86, v32
	v_cvt_f32_ubyte2_e32 v87, v32
	v_cvt_f32_ubyte3_e32 v88, v32
	v_fmac_f32_e32 v2, v85, v55
	v_fmac_f32_e32 v3, v86, v55
	v_fmac_f32_e32 v4, v87, v55
	v_fmac_f32_e32 v5, v88, v55
	v_cvt_f32_ubyte0_e32 v85, v33
	v_cvt_f32_ubyte1_e32 v86, v33
	v_cvt_f32_ubyte2_e32 v87, v33
	v_cvt_f32_ubyte3_e32 v88, v33
	v_fmac_f32_e32 v6, v85, v55
	v_fmac_f32_e32 v7, v86, v55
	v_fmac_f32_e32 v8, v87, v55
	v_fmac_f32_e32 v9, v88, v55
	v_cvt_f32_ubyte0_e32 v85, v34
	v_cvt_f32_ubyte1_e32 v86, v34
	v_cvt_f32_ubyte2_e32 v87, v34
	v_cvt_f32_ubyte3_e32 v88, v34
	v_fmac_f32_e32 v10, v85, v55
	v_fmac_f32_e32 v11, v86, v55
	v_fmac_f32_e32 v12, v87, v55
	v_fmac_f32_e32 v13, v88, v55
	v_cvt_f32_ubyte0_e32 v85, v35
	v_cvt_f32_ubyte1_e32 v86, v35
	v_cvt_f32_ubyte2_e32 v87, v35
	v_cvt_f32_ubyte3_e32 v88, v35
	v_fmac_f32_e32 v14, v85, v55
	v_fmac_f32_e32 v15, v86, v55
	v_fmac_f32_e32 v16, v87, v55
	v_fmac_f32_e32 v17, v88, v55
	v_lshrrev_b32_e32 v84, 16, v80
	v_lshl_or_b32 v83, v84, 7, v89
	v_cmp_lt_i32_e32 vcc, 19, v78
	s_mov_b64 exec, vcc
	global_load_dwordx4 v[32:35], v83, s[12:13]
	s_mov_b64 exec, -1
	v_cvt_f32_f16_sdwa v55, v82 dst_sel:DWORD dst_unused:UNUSED_PAD src0_sel:WORD_1
	s_cmp_le_u32 s40, 20
	s_cbranch_scc1 .Lg2_tail0
	s_waitcnt lgkmcnt(0)
	ds_bpermute_b32 v80, v90, v74 offset:12
	ds_bpermute_b32 v82, v90, v76 offset:12
	s_waitcnt vmcnt(3)
	v_cvt_f32_ubyte0_e32 v85, v20
	v_cvt_f32_ubyte1_e32 v86, v20
	v_cvt_f32_ubyte2_e32 v87, v20
	v_cvt_f32_ubyte3_e32 v88, v20
	v_fmac_f32_e32 v2, v85, v52
	v_fmac_f32_e32 v3, v86, v52
	v_fmac_f32_e32 v4, v87, v52
	v_fmac_f32_e32 v5, v88, v52
	v_cvt_f32_ubyte0_e32 v85, v21
	v_cvt_f32_ubyte1_e32 v86, v21
	v_cvt_f32_ubyte2_e32 v87, v21
	v_cvt_f32_ubyte3_e32 v88, v21
	v_fmac_f32_e32 v6, v85, v52
	v_fmac_f32_e32 v7, v86, v52
	v_fmac_f32_e32 v8, v87, v52
	v_fmac_f32_e32 v9, v88, v52
	v_cvt_f32_ubyte0_e32 v85, v22
	v_cvt_f32_ubyte1_e32 v86, v22
	v_cvt_f32_ubyte2_e32 v87, v22
	v_cvt_f32_ubyte3_e32 v88, v22
	v_fmac_f32_e32 v10, v85, v52
	v_fmac_f32_e32 v11, v86, v52
	v_fmac_f32_e32 v12, v87, v52
	v_fmac_f32_e32 v13, v88, v52
	v_cvt_f32_ubyte0_e32 v85, v23
	v_cvt_f32_ubyte1_e32 v86, v23
	v_cvt_f32_ubyte2_e32 v87, v23
	v_cvt_f32_ubyte3_e32 v88, v23
	v_fmac_f32_e32 v14, v85, v52
	v_fmac_f32_e32 v15, v86, v52
	v_fmac_f32_e32 v16, v87, v52
	v_fmac_f32_e32 v17, v88, v52
	v_and_b32_e32 v84, 0xffff, v79
	v_lshl_or_b32 v83, v84, 7, v89
	v_cmp_lt_i32_e32 vcc, 20, v78
	s_mov_b64 exec, vcc
	global_load_dwordx4 v[20:23], v83, s[12:13]
	s_mov_b64 exec, -1
	v_cvt_f32_f16_e32 v52, v81
	s_waitcnt vmcnt(3)
	v_cvt_f32_ubyte0_e32 v85, v24
	v_cvt_f32_ubyte1_e32 v86, v24
	v_cvt_f32_ubyte2_e32 v87, v24
	v_cvt_f32_ubyte3_e32 v88, v24
	v_fmac_f32_e32 v2, v85, v53
	v_fmac_f32_e32 v3, v86, v53
	v_fmac_f32_e32 v4, v87, v53
	v_fmac_f32_e32 v5, v88, v53
	v_cvt_f32_ubyte0_e32 v85, v25
	v_cvt_f32_ubyte1_e32 v86, v25
	v_cvt_f32_ubyte2_e32 v87, v25
	v_cvt_f32_ubyte3_e32 v88, v25
	v_fmac_f32_e32 v6, v85, v53
	v_fmac_f32_e32 v7, v86, v53
	v_fmac_f32_e32 v8, v87, v53
	v_fmac_f32_e32 v9, v88, v53
	v_cvt_f32_ubyte0_e32 v85, v26
	v_cvt_f32_ubyte1_e32 v86, v26
	v_cvt_f32_ubyte2_e32 v87, v26
	v_cvt_f32_ubyte3_e32 v88, v26
	v_fmac_f32_e32 v10, v85, v53
	v_fmac_f32_e32 v11, v86, v53
	v_fmac_f32_e32 v12, v87, v53
	v_fmac_f32_e32 v13, v88, v53
	v_cvt_f32_ubyte0_e32 v85, v27
	v_cvt_f32_ubyte1_e32 v86, v27
	v_cvt_f32_ubyte2_e32 v87, v27
	v_cvt_f32_ubyte3_e32 v88, v27
	v_fmac_f32_e32 v14, v85, v53
	v_fmac_f32_e32 v15, v86, v53
	v_fmac_f32_e32 v16, v87, v53
	v_fmac_f32_e32 v17, v88, v53
	v_lshrrev_b32_e32 v84, 16, v79
	v_lshl_or_b32 v83, v84, 7, v89
	v_cmp_lt_i32_e32 vcc, 21, v78
	s_mov_b64 exec, vcc
	global_load_dwordx4 v[24:27], v83, s[12:13]
	s_mov_b64 exec, -1
	v_cvt_f32_f16_sdwa v53, v81 dst_sel:DWORD dst_unused:UNUSED_PAD src0_sel:WORD_1
	s_waitcnt lgkmcnt(0)
	ds_bpermute_b32 v79, v90, v74 offset:16
	ds_bpermute_b32 v81, v90, v76 offset:16
	s_waitcnt vmcnt(3)
	v_cvt_f32_ubyte0_e32 v85, v28
	v_cvt_f32_ubyte1_e32 v86, v28
	v_cvt_f32_ubyte2_e32 v87, v28
	v_cvt_f32_ubyte3_e32 v88, v28
	v_fmac_f32_e32 v2, v85, v54
	v_fmac_f32_e32 v3, v86, v54
	v_fmac_f32_e32 v4, v87, v54
	v_fmac_f32_e32 v5, v88, v54
	v_cvt_f32_ubyte0_e32 v85, v29
	v_cvt_f32_ubyte1_e32 v86, v29
	v_cvt_f32_ubyte2_e32 v87, v29
	v_cvt_f32_ubyte3_e32 v88, v29
	v_fmac_f32_e32 v6, v85, v54
	v_fmac_f32_e32 v7, v86, v54
	v_fmac_f32_e32 v8, v87, v54
	v_fmac_f32_e32 v9, v88, v54
	v_cvt_f32_ubyte0_e32 v85, v30
	v_cvt_f32_ubyte1_e32 v86, v30
	v_cvt_f32_ubyte2_e32 v87, v30
	v_cvt_f32_ubyte3_e32 v88, v30
	v_fmac_f32_e32 v10, v85, v54
	v_fmac_f32_e32 v11, v86, v54
	v_fmac_f32_e32 v12, v87, v54
	v_fmac_f32_e32 v13, v88, v54
	v_cvt_f32_ubyte0_e32 v85, v31
	v_cvt_f32_ubyte1_e32 v86, v31
	v_cvt_f32_ubyte2_e32 v87, v31
	v_cvt_f32_ubyte3_e32 v88, v31
	v_fmac_f32_e32 v14, v85, v54
	v_fmac_f32_e32 v15, v86, v54
	v_fmac_f32_e32 v16, v87, v54
	v_fmac_f32_e32 v17, v88, v54
	v_and_b32_e32 v84, 0xffff, v80
	v_lshl_or_b32 v83, v84, 7, v89
	v_cmp_lt_i32_e32 vcc, 22, v78
	s_mov_b64 exec, vcc
	global_load_dwordx4 v[28:31], v83, s[12:13]
	s_mov_b64 exec, -1
	v_cvt_f32_f16_e32 v54, v82
	s_waitcnt vmcnt(3)
	v_cvt_f32_ubyte0_e32 v85, v32
	v_cvt_f32_ubyte1_e32 v86, v32
	v_cvt_f32_ubyte2_e32 v87, v32
	v_cvt_f32_ubyte3_e32 v88, v32
	v_fmac_f32_e32 v2, v85, v55
	v_fmac_f32_e32 v3, v86, v55
	v_fmac_f32_e32 v4, v87, v55
	v_fmac_f32_e32 v5, v88, v55
	v_cvt_f32_ubyte0_e32 v85, v33
	v_cvt_f32_ubyte1_e32 v86, v33
	v_cvt_f32_ubyte2_e32 v87, v33
	v_cvt_f32_ubyte3_e32 v88, v33
	v_fmac_f32_e32 v6, v85, v55
	v_fmac_f32_e32 v7, v86, v55
	v_fmac_f32_e32 v8, v87, v55
	v_fmac_f32_e32 v9, v88, v55
	v_cvt_f32_ubyte0_e32 v85, v34
	v_cvt_f32_ubyte1_e32 v86, v34
	v_cvt_f32_ubyte2_e32 v87, v34
	v_cvt_f32_ubyte3_e32 v88, v34
	v_fmac_f32_e32 v10, v85, v55
	v_fmac_f32_e32 v11, v86, v55
	v_fmac_f32_e32 v12, v87, v55
	v_fmac_f32_e32 v13, v88, v55
	v_cvt_f32_ubyte0_e32 v85, v35
	v_cvt_f32_ubyte1_e32 v86, v35
	v_cvt_f32_ubyte2_e32 v87, v35
	v_cvt_f32_ubyte3_e32 v88, v35
	v_fmac_f32_e32 v14, v85, v55
	v_fmac_f32_e32 v15, v86, v55
	v_fmac_f32_e32 v16, v87, v55
	v_fmac_f32_e32 v17, v88, v55
	v_lshrrev_b32_e32 v84, 16, v80
	v_lshl_or_b32 v83, v84, 7, v89
	v_cmp_lt_i32_e32 vcc, 23, v78
	s_mov_b64 exec, vcc
	global_load_dwordx4 v[32:35], v83, s[12:13]
	s_mov_b64 exec, -1
	v_cvt_f32_f16_sdwa v55, v82 dst_sel:DWORD dst_unused:UNUSED_PAD src0_sel:WORD_1
	s_cmp_le_u32 s40, 24
	s_cbranch_scc1 .Lg2_tail0
	s_waitcnt lgkmcnt(0)
	ds_bpermute_b32 v80, v90, v74 offset:20
	ds_bpermute_b32 v82, v90, v76 offset:20
	s_waitcnt vmcnt(3)
	v_cvt_f32_ubyte0_e32 v85, v20
	v_cvt_f32_ubyte1_e32 v86, v20
	v_cvt_f32_ubyte2_e32 v87, v20
	v_cvt_f32_ubyte3_e32 v88, v20
	v_fmac_f32_e32 v2, v85, v52
	v_fmac_f32_e32 v3, v86, v52
	v_fmac_f32_e32 v4, v87, v52
	v_fmac_f32_e32 v5, v88, v52
	v_cvt_f32_ubyte0_e32 v85, v21
	v_cvt_f32_ubyte1_e32 v86, v21
	v_cvt_f32_ubyte2_e32 v87, v21
	v_cvt_f32_ubyte3_e32 v88, v21
	v_fmac_f32_e32 v6, v85, v52
	v_fmac_f32_e32 v7, v86, v52
	v_fmac_f32_e32 v8, v87, v52
	v_fmac_f32_e32 v9, v88, v52
	v_cvt_f32_ubyte0_e32 v85, v22
	v_cvt_f32_ubyte1_e32 v86, v22
	v_cvt_f32_ubyte2_e32 v87, v22
	v_cvt_f32_ubyte3_e32 v88, v22
	v_fmac_f32_e32 v10, v85, v52
	v_fmac_f32_e32 v11, v86, v52
	v_fmac_f32_e32 v12, v87, v52
	v_fmac_f32_e32 v13, v88, v52
	v_cvt_f32_ubyte0_e32 v85, v23
	v_cvt_f32_ubyte1_e32 v86, v23
	v_cvt_f32_ubyte2_e32 v87, v23
	v_cvt_f32_ubyte3_e32 v88, v23
	v_fmac_f32_e32 v14, v85, v52
	v_fmac_f32_e32 v15, v86, v52
	v_fmac_f32_e32 v16, v87, v52
	v_fmac_f32_e32 v17, v88, v52
	v_and_b32_e32 v84, 0xffff, v79
	v_lshl_or_b32 v83, v84, 7, v89
	v_cmp_lt_i32_e32 vcc, 24, v78
	s_mov_b64 exec, vcc
	global_load_dwordx4 v[20:23], v83, s[12:13]
	s_mov_b64 exec, -1
	v_cvt_f32_f16_e32 v52, v81
	s_waitcnt vmcnt(3)
	v_cvt_f32_ubyte0_e32 v85, v24
	v_cvt_f32_ubyte1_e32 v86, v24
	v_cvt_f32_ubyte2_e32 v87, v24
	v_cvt_f32_ubyte3_e32 v88, v24
	v_fmac_f32_e32 v2, v85, v53
	v_fmac_f32_e32 v3, v86, v53
	v_fmac_f32_e32 v4, v87, v53
	v_fmac_f32_e32 v5, v88, v53
	v_cvt_f32_ubyte0_e32 v85, v25
	v_cvt_f32_ubyte1_e32 v86, v25
	v_cvt_f32_ubyte2_e32 v87, v25
	v_cvt_f32_ubyte3_e32 v88, v25
	v_fmac_f32_e32 v6, v85, v53
	v_fmac_f32_e32 v7, v86, v53
	v_fmac_f32_e32 v8, v87, v53
	v_fmac_f32_e32 v9, v88, v53
	v_cvt_f32_ubyte0_e32 v85, v26
	v_cvt_f32_ubyte1_e32 v86, v26
	v_cvt_f32_ubyte2_e32 v87, v26
	v_cvt_f32_ubyte3_e32 v88, v26
	v_fmac_f32_e32 v10, v85, v53
	v_fmac_f32_e32 v11, v86, v53
	v_fmac_f32_e32 v12, v87, v53
	v_fmac_f32_e32 v13, v88, v53
	v_cvt_f32_ubyte0_e32 v85, v27
	v_cvt_f32_ubyte1_e32 v86, v27
	v_cvt_f32_ubyte2_e32 v87, v27
	v_cvt_f32_ubyte3_e32 v88, v27
	v_fmac_f32_e32 v14, v85, v53
	v_fmac_f32_e32 v15, v86, v53
	v_fmac_f32_e32 v16, v87, v53
	v_fmac_f32_e32 v17, v88, v53
	v_lshrrev_b32_e32 v84, 16, v79
	v_lshl_or_b32 v83, v84, 7, v89
	v_cmp_lt_i32_e32 vcc, 25, v78
	s_mov_b64 exec, vcc
	global_load_dwordx4 v[24:27], v83, s[12:13]
	s_mov_b64 exec, -1
	v_cvt_f32_f16_sdwa v53, v81 dst_sel:DWORD dst_unused:UNUSED_PAD src0_sel:WORD_1
	s_waitcnt lgkmcnt(0)
	ds_bpermute_b32 v79, v90, v74 offset:24
	ds_bpermute_b32 v81, v90, v76 offset:24
	s_waitcnt vmcnt(3)
	v_cvt_f32_ubyte0_e32 v85, v28
	v_cvt_f32_ubyte1_e32 v86, v28
	v_cvt_f32_ubyte2_e32 v87, v28
	v_cvt_f32_ubyte3_e32 v88, v28
	v_fmac_f32_e32 v2, v85, v54
	v_fmac_f32_e32 v3, v86, v54
	v_fmac_f32_e32 v4, v87, v54
	v_fmac_f32_e32 v5, v88, v54
	v_cvt_f32_ubyte0_e32 v85, v29
	v_cvt_f32_ubyte1_e32 v86, v29
	v_cvt_f32_ubyte2_e32 v87, v29
	v_cvt_f32_ubyte3_e32 v88, v29
	v_fmac_f32_e32 v6, v85, v54
	v_fmac_f32_e32 v7, v86, v54
	v_fmac_f32_e32 v8, v87, v54
	v_fmac_f32_e32 v9, v88, v54
	v_cvt_f32_ubyte0_e32 v85, v30
	v_cvt_f32_ubyte1_e32 v86, v30
	v_cvt_f32_ubyte2_e32 v87, v30
	v_cvt_f32_ubyte3_e32 v88, v30
	v_fmac_f32_e32 v10, v85, v54
	v_fmac_f32_e32 v11, v86, v54
	v_fmac_f32_e32 v12, v87, v54
	v_fmac_f32_e32 v13, v88, v54
	v_cvt_f32_ubyte0_e32 v85, v31
	v_cvt_f32_ubyte1_e32 v86, v31
	v_cvt_f32_ubyte2_e32 v87, v31
	v_cvt_f32_ubyte3_e32 v88, v31
	v_fmac_f32_e32 v14, v85, v54
	v_fmac_f32_e32 v15, v86, v54
	v_fmac_f32_e32 v16, v87, v54
	v_fmac_f32_e32 v17, v88, v54
	v_and_b32_e32 v84, 0xffff, v80
	v_lshl_or_b32 v83, v84, 7, v89
	v_cmp_lt_i32_e32 vcc, 26, v78
	s_mov_b64 exec, vcc
	global_load_dwordx4 v[28:31], v83, s[12:13]
	s_mov_b64 exec, -1
	v_cvt_f32_f16_e32 v54, v82
	s_waitcnt vmcnt(3)
	v_cvt_f32_ubyte0_e32 v85, v32
	v_cvt_f32_ubyte1_e32 v86, v32
	v_cvt_f32_ubyte2_e32 v87, v32
	v_cvt_f32_ubyte3_e32 v88, v32
	v_fmac_f32_e32 v2, v85, v55
	v_fmac_f32_e32 v3, v86, v55
	v_fmac_f32_e32 v4, v87, v55
	v_fmac_f32_e32 v5, v88, v55
	v_cvt_f32_ubyte0_e32 v85, v33
	v_cvt_f32_ubyte1_e32 v86, v33
	v_cvt_f32_ubyte2_e32 v87, v33
	v_cvt_f32_ubyte3_e32 v88, v33
	v_fmac_f32_e32 v6, v85, v55
	v_fmac_f32_e32 v7, v86, v55
	v_fmac_f32_e32 v8, v87, v55
	v_fmac_f32_e32 v9, v88, v55
	v_cvt_f32_ubyte0_e32 v85, v34
	v_cvt_f32_ubyte1_e32 v86, v34
	v_cvt_f32_ubyte2_e32 v87, v34
	v_cvt_f32_ubyte3_e32 v88, v34
	v_fmac_f32_e32 v10, v85, v55
	v_fmac_f32_e32 v11, v86, v55
	v_fmac_f32_e32 v12, v87, v55
	v_fmac_f32_e32 v13, v88, v55
	v_cvt_f32_ubyte0_e32 v85, v35
	v_cvt_f32_ubyte1_e32 v86, v35
	v_cvt_f32_ubyte2_e32 v87, v35
	v_cvt_f32_ubyte3_e32 v88, v35
	v_fmac_f32_e32 v14, v85, v55
	v_fmac_f32_e32 v15, v86, v55
	v_fmac_f32_e32 v16, v87, v55
	v_fmac_f32_e32 v17, v88, v55
	v_lshrrev_b32_e32 v84, 16, v80
	v_lshl_or_b32 v83, v84, 7, v89
	v_cmp_lt_i32_e32 vcc, 27, v78
	s_mov_b64 exec, vcc
	global_load_dwordx4 v[32:35], v83, s[12:13]
	s_mov_b64 exec, -1
	v_cvt_f32_f16_sdwa v55, v82 dst_sel:DWORD dst_unused:UNUSED_PAD src0_sel:WORD_1
	s_cmp_le_u32 s40, 28
	s_cbranch_scc1 .Lg2_tail0
	s_waitcnt lgkmcnt(0)
	ds_bpermute_b32 v80, v90, v74 offset:28
	ds_bpermute_b32 v82, v90, v76 offset:28
	s_waitcnt vmcnt(3)
	v_cvt_f32_ubyte0_e32 v85, v20
	v_cvt_f32_ubyte1_e32 v86, v20
	v_cvt_f32_ubyte2_e32 v87, v20
	v_cvt_f32_ubyte3_e32 v88, v20
	v_fmac_f32_e32 v2, v85, v52
	v_fmac_f32_e32 v3, v86, v52
	v_fmac_f32_e32 v4, v87, v52
	v_fmac_f32_e32 v5, v88, v52
	v_cvt_f32_ubyte0_e32 v85, v21
	v_cvt_f32_ubyte1_e32 v86, v21
	v_cvt_f32_ubyte2_e32 v87, v21
	v_cvt_f32_ubyte3_e32 v88, v21
	v_fmac_f32_e32 v6, v85, v52
	v_fmac_f32_e32 v7, v86, v52
	v_fmac_f32_e32 v8, v87, v52
	v_fmac_f32_e32 v9, v88, v52
	v_cvt_f32_ubyte0_e32 v85, v22
	v_cvt_f32_ubyte1_e32 v86, v22
	v_cvt_f32_ubyte2_e32 v87, v22
	v_cvt_f32_ubyte3_e32 v88, v22
	v_fmac_f32_e32 v10, v85, v52
	v_fmac_f32_e32 v11, v86, v52
	v_fmac_f32_e32 v12, v87, v52
	v_fmac_f32_e32 v13, v88, v52
	v_cvt_f32_ubyte0_e32 v85, v23
	v_cvt_f32_ubyte1_e32 v86, v23
	v_cvt_f32_ubyte2_e32 v87, v23
	v_cvt_f32_ubyte3_e32 v88, v23
	v_fmac_f32_e32 v14, v85, v52
	v_fmac_f32_e32 v15, v86, v52
	v_fmac_f32_e32 v16, v87, v52
	v_fmac_f32_e32 v17, v88, v52
	v_and_b32_e32 v84, 0xffff, v79
	v_lshl_or_b32 v83, v84, 7, v89
	v_cmp_lt_i32_e32 vcc, 28, v78
	s_mov_b64 exec, vcc
	global_load_dwordx4 v[20:23], v83, s[12:13]
	s_mov_b64 exec, -1
	v_cvt_f32_f16_e32 v52, v81
	s_waitcnt vmcnt(3)
	v_cvt_f32_ubyte0_e32 v85, v24
	v_cvt_f32_ubyte1_e32 v86, v24
	v_cvt_f32_ubyte2_e32 v87, v24
	v_cvt_f32_ubyte3_e32 v88, v24
	v_fmac_f32_e32 v2, v85, v53
	v_fmac_f32_e32 v3, v86, v53
	v_fmac_f32_e32 v4, v87, v53
	v_fmac_f32_e32 v5, v88, v53
	v_cvt_f32_ubyte0_e32 v85, v25
	v_cvt_f32_ubyte1_e32 v86, v25
	v_cvt_f32_ubyte2_e32 v87, v25
	v_cvt_f32_ubyte3_e32 v88, v25
	v_fmac_f32_e32 v6, v85, v53
	v_fmac_f32_e32 v7, v86, v53
	v_fmac_f32_e32 v8, v87, v53
	v_fmac_f32_e32 v9, v88, v53
	v_cvt_f32_ubyte0_e32 v85, v26
	v_cvt_f32_ubyte1_e32 v86, v26
	v_cvt_f32_ubyte2_e32 v87, v26
	v_cvt_f32_ubyte3_e32 v88, v26
	v_fmac_f32_e32 v10, v85, v53
	v_fmac_f32_e32 v11, v86, v53
	v_fmac_f32_e32 v12, v87, v53
	v_fmac_f32_e32 v13, v88, v53
	v_cvt_f32_ubyte0_e32 v85, v27
	v_cvt_f32_ubyte1_e32 v86, v27
	v_cvt_f32_ubyte2_e32 v87, v27
	v_cvt_f32_ubyte3_e32 v88, v27
	v_fmac_f32_e32 v14, v85, v53
	v_fmac_f32_e32 v15, v86, v53
	v_fmac_f32_e32 v16, v87, v53
	v_fmac_f32_e32 v17, v88, v53
	v_lshrrev_b32_e32 v84, 16, v79
	v_lshl_or_b32 v83, v84, 7, v89
	v_cmp_lt_i32_e32 vcc, 29, v78
	s_mov_b64 exec, vcc
	global_load_dwordx4 v[24:27], v83, s[12:13]
	s_mov_b64 exec, -1
	v_cvt_f32_f16_sdwa v53, v81 dst_sel:DWORD dst_unused:UNUSED_PAD src0_sel:WORD_1
	s_waitcnt lgkmcnt(0)
	s_waitcnt vmcnt(3)
	v_cvt_f32_ubyte0_e32 v85, v28
	v_cvt_f32_ubyte1_e32 v86, v28
	v_cvt_f32_ubyte2_e32 v87, v28
	v_cvt_f32_ubyte3_e32 v88, v28
	v_fmac_f32_e32 v2, v85, v54
	v_fmac_f32_e32 v3, v86, v54
	v_fmac_f32_e32 v4, v87, v54
	v_fmac_f32_e32 v5, v88, v54
	v_cvt_f32_ubyte0_e32 v85, v29
	v_cvt_f32_ubyte1_e32 v86, v29
	v_cvt_f32_ubyte2_e32 v87, v29
	v_cvt_f32_ubyte3_e32 v88, v29
	v_fmac_f32_e32 v6, v85, v54
	v_fmac_f32_e32 v7, v86, v54
	v_fmac_f32_e32 v8, v87, v54
	v_fmac_f32_e32 v9, v88, v54
	v_cvt_f32_ubyte0_e32 v85, v30
	v_cvt_f32_ubyte1_e32 v86, v30
	v_cvt_f32_ubyte2_e32 v87, v30
	v_cvt_f32_ubyte3_e32 v88, v30
	v_fmac_f32_e32 v10, v85, v54
	v_fmac_f32_e32 v11, v86, v54
	v_fmac_f32_e32 v12, v87, v54
	v_fmac_f32_e32 v13, v88, v54
	v_cvt_f32_ubyte0_e32 v85, v31
	v_cvt_f32_ubyte1_e32 v86, v31
	v_cvt_f32_ubyte2_e32 v87, v31
	v_cvt_f32_ubyte3_e32 v88, v31
	v_fmac_f32_e32 v14, v85, v54
	v_fmac_f32_e32 v15, v86, v54
	v_fmac_f32_e32 v16, v87, v54
	v_fmac_f32_e32 v17, v88, v54
	v_and_b32_e32 v84, 0xffff, v80
	v_lshl_or_b32 v83, v84, 7, v89
	v_cmp_lt_i32_e32 vcc, 30, v78
	s_mov_b64 exec, vcc
	global_load_dwordx4 v[28:31], v83, s[12:13]
	s_mov_b64 exec, -1
	v_cvt_f32_f16_e32 v54, v82
	s_waitcnt vmcnt(3)
	v_cvt_f32_ubyte0_e32 v85, v32
	v_cvt_f32_ubyte1_e32 v86, v32
	v_cvt_f32_ubyte2_e32 v87, v32
	v_cvt_f32_ubyte3_e32 v88, v32
	v_fmac_f32_e32 v2, v85, v55
	v_fmac_f32_e32 v3, v86, v55
	v_fmac_f32_e32 v4, v87, v55
	v_fmac_f32_e32 v5, v88, v55
	v_cvt_f32_ubyte0_e32 v85, v33
	v_cvt_f32_ubyte1_e32 v86, v33
	v_cvt_f32_ubyte2_e32 v87, v33
	v_cvt_f32_ubyte3_e32 v88, v33
	v_fmac_f32_e32 v6, v85, v55
	v_fmac_f32_e32 v7, v86, v55
	v_fmac_f32_e32 v8, v87, v55
	v_fmac_f32_e32 v9, v88, v55
	v_cvt_f32_ubyte0_e32 v85, v34
	v_cvt_f32_ubyte1_e32 v86, v34
	v_cvt_f32_ubyte2_e32 v87, v34
	v_cvt_f32_ubyte3_e32 v88, v34
	v_fmac_f32_e32 v10, v85, v55
	v_fmac_f32_e32 v11, v86, v55
	v_fmac_f32_e32 v12, v87, v55
	v_fmac_f32_e32 v13, v88, v55
	v_cvt_f32_ubyte0_e32 v85, v35
	v_cvt_f32_ubyte1_e32 v86, v35
	v_cvt_f32_ubyte2_e32 v87, v35
	v_cvt_f32_ubyte3_e32 v88, v35
	v_fmac_f32_e32 v14, v85, v55
	v_fmac_f32_e32 v15, v86, v55
	v_fmac_f32_e32 v16, v87, v55
	v_fmac_f32_e32 v17, v88, v55
	v_lshrrev_b32_e32 v84, 16, v80
	v_lshl_or_b32 v83, v84, 7, v89
	v_cmp_lt_i32_e32 vcc, 31, v78
	s_mov_b64 exec, vcc
	global_load_dwordx4 v[32:35], v83, s[12:13]
	s_mov_b64 exec, -1
	v_cvt_f32_f16_sdwa v55, v82 dst_sel:DWORD dst_unused:UNUSED_PAD src0_sel:WORD_1
.Lg2_tail0:
	s_cmp_eq_u32 s39, 1
	s_cbranch_scc1 .Lg2_tailb0
	s_waitcnt vmcnt(3)
	v_cvt_f32_ubyte0_e32 v85, v20
	v_cvt_f32_ubyte1_e32 v86, v20
	v_cvt_f32_ubyte2_e32 v87, v20
	v_cvt_f32_ubyte3_e32 v88, v20
	v_fmac_f32_e32 v2, v85, v52
	v_fmac_f32_e32 v3, v86, v52
	v_fmac_f32_e32 v4, v87, v52
	v_fmac_f32_e32 v5, v88, v52
	v_cvt_f32_ubyte0_e32 v85, v21
	v_cvt_f32_ubyte1_e32 v86, v21
	v_cvt_f32_ubyte2_e32 v87, v21
	v_cvt_f32_ubyte3_e32 v88, v21
	v_fmac_f32_e32 v6, v85, v52
	v_fmac_f32_e32 v7, v86, v52
	v_fmac_f32_e32 v8, v87, v52
	v_fmac_f32_e32 v9, v88, v52
	v_cvt_f32_ubyte0_e32 v85, v22
	v_cvt_f32_ubyte1_e32 v86, v22
	v_cvt_f32_ubyte2_e32 v87, v22
	v_cvt_f32_ubyte3_e32 v88, v22
	v_fmac_f32_e32 v10, v85, v52
	v_fmac_f32_e32 v11, v86, v52
	v_fmac_f32_e32 v12, v87, v52
	v_fmac_f32_e32 v13, v88, v52
	v_cvt_f32_ubyte0_e32 v85, v23
	v_cvt_f32_ubyte1_e32 v86, v23
	v_cvt_f32_ubyte2_e32 v87, v23
	v_cvt_f32_ubyte3_e32 v88, v23
	v_fmac_f32_e32 v14, v85, v52
	v_fmac_f32_e32 v15, v86, v52
	v_fmac_f32_e32 v16, v87, v52
	v_fmac_f32_e32 v17, v88, v52
	s_waitcnt vmcnt(2)
	v_cvt_f32_ubyte0_e32 v85, v24
	v_cvt_f32_ubyte1_e32 v86, v24
	v_cvt_f32_ubyte2_e32 v87, v24
	v_cvt_f32_ubyte3_e32 v88, v24
	v_fmac_f32_e32 v2, v85, v53
	v_fmac_f32_e32 v3, v86, v53
	v_fmac_f32_e32 v4, v87, v53
	v_fmac_f32_e32 v5, v88, v53
	v_cvt_f32_ubyte0_e32 v85, v25
	v_cvt_f32_ubyte1_e32 v86, v25
	v_cvt_f32_ubyte2_e32 v87, v25
	v_cvt_f32_ubyte3_e32 v88, v25
	v_fmac_f32_e32 v6, v85, v53
	v_fmac_f32_e32 v7, v86, v53
	v_fmac_f32_e32 v8, v87, v53
	v_fmac_f32_e32 v9, v88, v53
	v_cvt_f32_ubyte0_e32 v85, v26
	v_cvt_f32_ubyte1_e32 v86, v26
	v_cvt_f32_ubyte2_e32 v87, v26
	v_cvt_f32_ubyte3_e32 v88, v26
	v_fmac_f32_e32 v10, v85, v53
	v_fmac_f32_e32 v11, v86, v53
	v_fmac_f32_e32 v12, v87, v53
	v_fmac_f32_e32 v13, v88, v53
	v_cvt_f32_ubyte0_e32 v85, v27
	v_cvt_f32_ubyte1_e32 v86, v27
	v_cvt_f32_ubyte2_e32 v87, v27
	v_cvt_f32_ubyte3_e32 v88, v27
	v_fmac_f32_e32 v14, v85, v53
	v_fmac_f32_e32 v15, v86, v53
	v_fmac_f32_e32 v16, v87, v53
	v_fmac_f32_e32 v17, v88, v53
	s_waitcnt vmcnt(1)
	v_cvt_f32_ubyte0_e32 v85, v28
	v_cvt_f32_ubyte1_e32 v86, v28
	v_cvt_f32_ubyte2_e32 v87, v28
	v_cvt_f32_ubyte3_e32 v88, v28
	v_fmac_f32_e32 v2, v85, v54
	v_fmac_f32_e32 v3, v86, v54
	v_fmac_f32_e32 v4, v87, v54
	v_fmac_f32_e32 v5, v88, v54
	v_cvt_f32_ubyte0_e32 v85, v29
	v_cvt_f32_ubyte1_e32 v86, v29
	v_cvt_f32_ubyte2_e32 v87, v29
	v_cvt_f32_ubyte3_e32 v88, v29
	v_fmac_f32_e32 v6, v85, v54
	v_fmac_f32_e32 v7, v86, v54
	v_fmac_f32_e32 v8, v87, v54
	v_fmac_f32_e32 v9, v88, v54
	v_cvt_f32_ubyte0_e32 v85, v30
	v_cvt_f32_ubyte1_e32 v86, v30
	v_cvt_f32_ubyte2_e32 v87, v30
	v_cvt_f32_ubyte3_e32 v88, v30
	v_fmac_f32_e32 v10, v85, v54
	v_fmac_f32_e32 v11, v86, v54
	v_fmac_f32_e32 v12, v87, v54
	v_fmac_f32_e32 v13, v88, v54
	v_cvt_f32_ubyte0_e32 v85, v31
	v_cvt_f32_ubyte1_e32 v86, v31
	v_cvt_f32_ubyte2_e32 v87, v31
	v_cvt_f32_ubyte3_e32 v88, v31
	v_fmac_f32_e32 v14, v85, v54
	v_fmac_f32_e32 v15, v86, v54
	v_fmac_f32_e32 v16, v87, v54
	v_fmac_f32_e32 v17, v88, v54
	s_waitcnt vmcnt(0)
	v_cvt_f32_ubyte0_e32 v85, v32
	v_cvt_f32_ubyte1_e32 v86, v32
	v_cvt_f32_ubyte2_e32 v87, v32
	v_cvt_f32_ubyte3_e32 v88, v32
	v_fmac_f32_e32 v2, v85, v55
	v_fmac_f32_e32 v3, v86, v55
	v_fmac_f32_e32 v4, v87, v55
	v_fmac_f32_e32 v5, v88, v55
	v_cvt_f32_ubyte0_e32 v85, v33
	v_cvt_f32_ubyte1_e32 v86, v33
	v_cvt_f32_ubyte2_e32 v87, v33
	v_cvt_f32_ubyte3_e32 v88, v33
	v_fmac_f32_e32 v6, v85, v55
	v_fmac_f32_e32 v7, v86, v55
	v_fmac_f32_e32 v8, v87, v55
	v_fmac_f32_e32 v9, v88, v55
	v_cvt_f32_ubyte0_e32 v85, v34
	v_cvt_f32_ubyte1_e32 v86, v34
	v_cvt_f32_ubyte2_e32 v87, v34
	v_cvt_f32_ubyte3_e32 v88, v34
	v_fmac_f32_e32 v10, v85, v55
	v_fmac_f32_e32 v11, v86, v55
	v_fmac_f32_e32 v12, v87, v55
	v_fmac_f32_e32 v13, v88, v55
	v_cvt_f32_ubyte0_e32 v85, v35
	v_cvt_f32_ubyte1_e32 v86, v35
	v_cvt_f32_ubyte2_e32 v87, v35
	v_cvt_f32_ubyte3_e32 v88, v35
	v_fmac_f32_e32 v14, v85, v55
	v_fmac_f32_e32 v15, v86, v55
	v_fmac_f32_e32 v16, v87, v55
	v_fmac_f32_e32 v17, v88, v55
	s_branch .Lg2_rare_check
.Lg2_tailb0:
	s_waitcnt vmcnt(3)
	v_cvt_f32_ubyte0_e32 v85, v20
	v_cvt_f32_ubyte1_e32 v86, v20
	v_cvt_f32_ubyte2_e32 v87, v20
	v_cvt_f32_ubyte3_e32 v88, v20
	v_fmac_f32_e32 v2, v85, v52
	v_fmac_f32_e32 v3, v86, v52
	v_fmac_f32_e32 v4, v87, v52
	v_fmac_f32_e32 v5, v88, v52
	v_cvt_f32_ubyte0_e32 v85, v21
	v_cvt_f32_ubyte1_e32 v86, v21
	v_cvt_f32_ubyte2_e32 v87, v21
	v_cvt_f32_ubyte3_e32 v88, v21
	v_fmac_f32_e32 v6, v85, v52
	v_fmac_f32_e32 v7, v86, v52
	v_fmac_f32_e32 v8, v87, v52
	v_fmac_f32_e32 v9, v88, v52
	v_cvt_f32_ubyte0_e32 v85, v22
	v_cvt_f32_ubyte1_e32 v86, v22
	v_cvt_f32_ubyte2_e32 v87, v22
	v_cvt_f32_ubyte3_e32 v88, v22
	v_fmac_f32_e32 v10, v85, v52
	v_fmac_f32_e32 v11, v86, v52
	v_fmac_f32_e32 v12, v87, v52
	v_fmac_f32_e32 v13, v88, v52
	v_cvt_f32_ubyte0_e32 v85, v23
	v_cvt_f32_ubyte1_e32 v86, v23
	v_cvt_f32_ubyte2_e32 v87, v23
	v_cvt_f32_ubyte3_e32 v88, v23
	v_fmac_f32_e32 v14, v85, v52
	v_fmac_f32_e32 v15, v86, v52
	v_fmac_f32_e32 v16, v87, v52
	v_fmac_f32_e32 v17, v88, v52
	global_load_dwordx4 v[112:115], v103, s[10:11] offset:0
	s_waitcnt vmcnt(3)
	v_cvt_f32_ubyte0_e32 v85, v24
	v_cvt_f32_ubyte1_e32 v86, v24
	v_cvt_f32_ubyte2_e32 v87, v24
	v_cvt_f32_ubyte3_e32 v88, v24
	v_fmac_f32_e32 v2, v85, v53
	v_fmac_f32_e32 v3, v86, v53
	v_fmac_f32_e32 v4, v87, v53
	v_fmac_f32_e32 v5, v88, v53
	v_cvt_f32_ubyte0_e32 v85, v25
	v_cvt_f32_ubyte1_e32 v86, v25
	v_cvt_f32_ubyte2_e32 v87, v25
	v_cvt_f32_ubyte3_e32 v88, v25
	v_fmac_f32_e32 v6, v85, v53
	v_fmac_f32_e32 v7, v86, v53
	v_fmac_f32_e32 v8, v87, v53
	v_fmac_f32_e32 v9, v88, v53
	v_cvt_f32_ubyte0_e32 v85, v26
	v_cvt_f32_ubyte1_e32 v86, v26
	v_cvt_f32_ubyte2_e32 v87, v26
	v_cvt_f32_ubyte3_e32 v88, v26
	v_fmac_f32_e32 v10, v85, v53
	v_fmac_f32_e32 v11, v86, v53
	v_fmac_f32_e32 v12, v87, v53
	v_fmac_f32_e32 v13, v88, v53
	v_cvt_f32_ubyte0_e32 v85, v27
	v_cvt_f32_ubyte1_e32 v86, v27
	v_cvt_f32_ubyte2_e32 v87, v27
	v_cvt_f32_ubyte3_e32 v88, v27
	v_fmac_f32_e32 v14, v85, v53
	v_fmac_f32_e32 v15, v86, v53
	v_fmac_f32_e32 v16, v87, v53
	v_fmac_f32_e32 v17, v88, v53
	global_load_dwordx4 v[116:119], v103, s[10:11] offset:64
	s_waitcnt vmcnt(3)
	v_cvt_f32_ubyte0_e32 v85, v28
	v_cvt_f32_ubyte1_e32 v86, v28
	v_cvt_f32_ubyte2_e32 v87, v28
	v_cvt_f32_ubyte3_e32 v88, v28
	v_fmac_f32_e32 v2, v85, v54
	v_fmac_f32_e32 v3, v86, v54
	v_fmac_f32_e32 v4, v87, v54
	v_fmac_f32_e32 v5, v88, v54
	v_cvt_f32_ubyte0_e32 v85, v29
	v_cvt_f32_ubyte1_e32 v86, v29
	v_cvt_f32_ubyte2_e32 v87, v29
	v_cvt_f32_ubyte3_e32 v88, v29
	v_fmac_f32_e32 v6, v85, v54
	v_fmac_f32_e32 v7, v86, v54
	v_fmac_f32_e32 v8, v87, v54
	v_fmac_f32_e32 v9, v88, v54
	v_cvt_f32_ubyte0_e32 v85, v30
	v_cvt_f32_ubyte1_e32 v86, v30
	v_cvt_f32_ubyte2_e32 v87, v30
	v_cvt_f32_ubyte3_e32 v88, v30
	v_fmac_f32_e32 v10, v85, v54
	v_fmac_f32_e32 v11, v86, v54
	v_fmac_f32_e32 v12, v87, v54
	v_fmac_f32_e32 v13, v88, v54
	v_cvt_f32_ubyte0_e32 v85, v31
	v_cvt_f32_ubyte1_e32 v86, v31
	v_cvt_f32_ubyte2_e32 v87, v31
	v_cvt_f32_ubyte3_e32 v88, v31
	v_fmac_f32_e32 v14, v85, v54
	v_fmac_f32_e32 v15, v86, v54
	v_fmac_f32_e32 v16, v87, v54
	v_fmac_f32_e32 v17, v88, v54
	global_load_dwordx4 v[120:123], v103, s[10:11] offset:128
	s_waitcnt vmcnt(3)
	v_cvt_f32_ubyte0_e32 v85, v32
	v_cvt_f32_ubyte1_e32 v86, v32
	v_cvt_f32_ubyte2_e32 v87, v32
	v_cvt_f32_ubyte3_e32 v88, v32
	v_fmac_f32_e32 v2, v85, v55
	v_fmac_f32_e32 v3, v86, v55
	v_fmac_f32_e32 v4, v87, v55
	v_fmac_f32_e32 v5, v88, v55
	v_cvt_f32_ubyte0_e32 v85, v33
	v_cvt_f32_ubyte1_e32 v86, v33
	v_cvt_f32_ubyte2_e32 v87, v33
	v_cvt_f32_ubyte3_e32 v88, v33
	v_fmac_f32_e32 v6, v85, v55
	v_fmac_f32_e32 v7, v86, v55
	v_fmac_f32_e32 v8, v87, v55
	v_fmac_f32_e32 v9, v88, v55
	v_cvt_f32_ubyte0_e32 v85, v34
	v_cvt_f32_ubyte1_e32 v86, v34
	v_cvt_f32_ubyte2_e32 v87, v34
	v_cvt_f32_ubyte3_e32 v88, v34
	v_fmac_f32_e32 v10, v85, v55
	v_fmac_f32_e32 v11, v86, v55
	v_fmac_f32_e32 v12, v87, v55
	v_fmac_f32_e32 v13, v88, v55
	v_cvt_f32_ubyte0_e32 v85, v35
	v_cvt_f32_ubyte1_e32 v86, v35
	v_cvt_f32_ubyte2_e32 v87, v35
	v_cvt_f32_ubyte3_e32 v88, v35
	v_fmac_f32_e32 v14, v85, v55
	v_fmac_f32_e32 v15, v86, v55
	v_fmac_f32_e32 v16, v87, v55
	v_fmac_f32_e32 v17, v88, v55
	global_load_dwordx4 v[124:127], v103, s[10:11] offset:192
	s_branch .Lg2_rare_check
